# previous + MoE GEMM units after the first start their accumulators from an inline-zero C operand (no per-unit accumulator clearing)
# baseline (speedup 1.0000x reference)
;     ...
;         if (Epi::NST > 0 && ui > 0) { PG_KPAIR(0, 8 + Epi::NST); t0 = 2; }
.LBB0_1995:
	s_cmp_lt_i32 s88, 1
	v_add_u32_e32 v51, 0x10000, v226
	v_add_u32_e32 v52, 0x14000, v226
	v_add_u32_e32 v53, 0x18000, v226
	v_add_u32_e32 v229, 0x1c000, v226
	s_cbranch_scc1 .LBB0_1997
	ds_read_b128 v[2:5], v51
	ds_read_b128 v[6:9], v51 offset:1024
	ds_read_b128 v[10:13], v51 offset:2048
	ds_read_b128 v[14:17], v51 offset:3072
	ds_read_b128 v[18:21], v52
	ds_read_b128 v[22:25], v52 offset:1024
	ds_read_b128 v[26:29], v52 offset:2048
	ds_read_b128 v[30:33], v52 offset:3072
	s_add_u32 s26, s6, 0x100
	s_addc_u32 s27, s7, 0
	ds_read_b128 v[34:37], v227
	ds_read_b128 v[38:41], v227 offset:1024
	ds_read_b128 v[42:45], v227 offset:2048
	ds_read_b128 v[46:49], v227 offset:3072
	ds_read_b128 v[182:185], v227 offset:4096
	ds_read_b128 v[186:189], v227 offset:5120
	ds_read_b128 v[190:193], v227 offset:6144
	ds_read_b128 v[194:197], v227 offset:7168
	s_mov_b32 m0, s62
	s_nop 0
	global_load_lds_dwordx4 v220, s[8:9]
	s_nop 0
	s_mov_b32 m0, s63
	s_nop 0
	global_load_lds_dwordx4 v222, s[8:9]
	s_waitcnt vmcnt(16)
	s_waitcnt lgkmcnt(0)
	s_barrier
	s_setprio 1
	v_mfma_scale_f32_16x16x128_f8f6f4 v[178:181], v[2:7], v[34:39], 0, v8, v40 op_sel_hi:[0,0,0] cbsz:2 blgp:2
	v_mfma_scale_f32_16x16x128_f8f6f4 v[174:177], v[10:15], v[34:39], 0, v16, v40 op_sel_hi:[0,0,0] cbsz:2 blgp:2
	v_mfma_scale_f32_16x16x128_f8f6f4 v[170:173], v[2:7], v[42:47], 0, v8, v48 op_sel_hi:[0,0,0] cbsz:2 blgp:2
	v_mfma_scale_f32_16x16x128_f8f6f4 v[166:169], v[10:15], v[42:47], 0, v16, v48 op_sel_hi:[0,0,0] cbsz:2 blgp:2
	v_mfma_scale_f32_16x16x128_f8f6f4 v[162:165], v[2:7], v[182:187], 0, v8, v188 op_sel_hi:[0,0,0] cbsz:2 blgp:2
	v_mfma_scale_f32_16x16x128_f8f6f4 v[158:161], v[10:15], v[182:187], 0, v16, v188 op_sel_hi:[0,0,0] cbsz:2 blgp:2
	v_mfma_scale_f32_16x16x128_f8f6f4 v[154:157], v[2:7], v[190:195], 0, v8, v196 op_sel_hi:[0,0,0] cbsz:2 blgp:2
	v_mfma_scale_f32_16x16x128_f8f6f4 v[150:153], v[10:15], v[190:195], 0, v16, v196 op_sel_hi:[0,0,0] cbsz:2 blgp:2
	v_mfma_scale_f32_16x16x128_f8f6f4 v[146:149], v[18:23], v[34:39], 0, v24, v40 op_sel_hi:[0,0,0] cbsz:2 blgp:2
	v_mfma_scale_f32_16x16x128_f8f6f4 v[142:145], v[26:31], v[34:39], 0, v32, v40 op_sel_hi:[0,0,0] cbsz:2 blgp:2
	v_mfma_scale_f32_16x16x128_f8f6f4 v[138:141], v[18:23], v[42:47], 0, v24, v48 op_sel_hi:[0,0,0] cbsz:2 blgp:2
	v_mfma_scale_f32_16x16x128_f8f6f4 v[134:137], v[26:31], v[42:47], 0, v32, v48 op_sel_hi:[0,0,0] cbsz:2 blgp:2
	v_mfma_scale_f32_16x16x128_f8f6f4 v[130:133], v[18:23], v[182:187], 0, v24, v188 op_sel_hi:[0,0,0] cbsz:2 blgp:2
	v_mfma_scale_f32_16x16x128_f8f6f4 v[126:129], v[26:31], v[182:187], 0, v32, v188 op_sel_hi:[0,0,0] cbsz:2 blgp:2
	v_mfma_scale_f32_16x16x128_f8f6f4 v[122:125], v[18:23], v[190:195], 0, v24, v196 op_sel_hi:[0,0,0] cbsz:2 blgp:2
	v_mfma_scale_f32_16x16x128_f8f6f4 v[118:121], v[26:31], v[190:195], 0, v32, v196 op_sel_hi:[0,0,0] cbsz:2 blgp:2
	s_setprio 0
	s_barrier
	ds_read_b128 v[34:37], v227 offset:16384
	ds_read_b128 v[38:41], v227 offset:17408
	ds_read_b128 v[42:45], v227 offset:18432
	ds_read_b128 v[46:49], v227 offset:19456
	ds_read_b128 v[182:185], v227 offset:20480
	ds_read_b128 v[186:189], v227 offset:21504
	ds_read_b128 v[190:193], v227 offset:22528
	ds_read_b128 v[194:197], v227 offset:23552
	s_mov_b32 m0, s47
	s_nop 0
	global_load_lds_dwordx4 v219, s[10:11]
	s_nop 0
	s_mov_b32 m0, s53
	s_nop 0
	global_load_lds_dwordx4 v221, s[10:11]
	s_waitcnt vmcnt(12)
	s_waitcnt lgkmcnt(0)
	s_barrier
	s_setprio 1
	v_mfma_scale_f32_16x16x128_f8f6f4 v[114:117], v[2:7], v[34:39], 0, v8, v40 op_sel_hi:[0,0,0] cbsz:2 blgp:2
	v_mfma_scale_f32_16x16x128_f8f6f4 v[110:113], v[10:15], v[34:39], 0, v16, v40 op_sel_hi:[0,0,0] cbsz:2 blgp:2
	s_mov_b32 m0, s48
	s_nop 0
	global_load_lds_dwordx4 v214, s[26:27]
	v_mfma_scale_f32_16x16x128_f8f6f4 v[106:109], v[2:7], v[42:47], 0, v8, v48 op_sel_hi:[0,0,0] cbsz:2 blgp:2
	v_mfma_scale_f32_16x16x128_f8f6f4 v[102:105], v[10:15], v[42:47], 0, v16, v48 op_sel_hi:[0,0,0] cbsz:2 blgp:2
	s_mov_b32 m0, s49
	s_nop 0
	global_load_lds_dwordx4 v215, s[26:27]
	s_add_u32 s26, s6, 0x40100
	s_addc_u32 s27, s7, 0
	v_mfma_scale_f32_16x16x128_f8f6f4 v[98:101], v[2:7], v[182:187], 0, v8, v188 op_sel_hi:[0,0,0] cbsz:2 blgp:2
	v_mfma_scale_f32_16x16x128_f8f6f4 v[94:97], v[10:15], v[182:187], 0, v16, v188 op_sel_hi:[0,0,0] cbsz:2 blgp:2
	v_mfma_scale_f32_16x16x128_f8f6f4 v[90:93], v[2:7], v[190:195], 0, v8, v196 op_sel_hi:[0,0,0] cbsz:2 blgp:2
	v_mfma_scale_f32_16x16x128_f8f6f4 v[86:89], v[10:15], v[190:195], 0, v16, v196 op_sel_hi:[0,0,0] cbsz:2 blgp:2
	v_mfma_scale_f32_16x16x128_f8f6f4 v[82:85], v[18:23], v[34:39], 0, v24, v40 op_sel_hi:[0,0,0] cbsz:2 blgp:2
	v_mfma_scale_f32_16x16x128_f8f6f4 v[78:81], v[26:31], v[34:39], 0, v32, v40 op_sel_hi:[0,0,0] cbsz:2 blgp:2
	s_mov_b32 m0, s51
	s_nop 0
	global_load_lds_dwordx4 v214, s[26:27]
	v_mfma_scale_f32_16x16x128_f8f6f4 v[74:77], v[18:23], v[42:47], 0, v24, v48 op_sel_hi:[0,0,0] cbsz:2 blgp:2
	v_mfma_scale_f32_16x16x128_f8f6f4 v[70:73], v[26:31], v[42:47], 0, v32, v48 op_sel_hi:[0,0,0] cbsz:2 blgp:2
	s_mov_b32 m0, s52
	s_nop 0
	global_load_lds_dwordx4 v215, s[26:27]
	v_mfma_scale_f32_16x16x128_f8f6f4 v[66:69], v[18:23], v[182:187], 0, v24, v188 op_sel_hi:[0,0,0] cbsz:2 blgp:2
	v_mfma_scale_f32_16x16x128_f8f6f4 v[62:65], v[26:31], v[182:187], 0, v32, v188 op_sel_hi:[0,0,0] cbsz:2 blgp:2
	v_mfma_scale_f32_16x16x128_f8f6f4 v[58:61], v[18:23], v[190:195], 0, v24, v196 op_sel_hi:[0,0,0] cbsz:2 blgp:2
	v_mfma_scale_f32_16x16x128_f8f6f4 v[54:57], v[26:31], v[190:195], 0, v32, v196 op_sel_hi:[0,0,0] cbsz:2 blgp:2
	s_setprio 0
	s_barrier
	ds_read_b128 v[2:5], v53
	ds_read_b128 v[6:9], v53 offset:1024
	ds_read_b128 v[10:13], v53 offset:2048
	ds_read_b128 v[14:17], v53 offset:3072
	ds_read_b128 v[18:21], v229
	ds_read_b128 v[22:25], v229 offset:1024
	ds_read_b128 v[26:29], v229 offset:2048
	ds_read_b128 v[30:33], v229 offset:3072
	ds_read_b128 v[34:37], v227 offset:32768
	ds_read_b128 v[38:41], v227 offset:33792
	ds_read_b128 v[42:45], v227 offset:34816
	ds_read_b128 v[46:49], v227 offset:35840
	ds_read_b128 v[182:185], v227 offset:36864
	ds_read_b128 v[186:189], v227 offset:37888
	ds_read_b128 v[190:193], v227 offset:38912
	ds_read_b128 v[194:197], v227 offset:39936
	s_mov_b32 m0, s54
	s_nop 0
	global_load_lds_dwordx4 v220, s[10:11]
	s_nop 0
	s_mov_b32 m0, s55
	s_nop 0
	global_load_lds_dwordx4 v222, s[10:11]
	s_waitcnt vmcnt(8)
	s_waitcnt lgkmcnt(0)
	s_barrier
	s_setprio 1
	v_mfma_scale_f32_16x16x128_f8f6f4 v[178:181], v[2:7], v[34:39], v[178:181], v8, v40 op_sel_hi:[0,0,0] cbsz:2 blgp:2
	v_mfma_scale_f32_16x16x128_f8f6f4 v[174:177], v[10:15], v[34:39], v[174:177], v16, v40 op_sel_hi:[0,0,0] cbsz:2 blgp:2
	v_mfma_scale_f32_16x16x128_f8f6f4 v[170:173], v[2:7], v[42:47], v[170:173], v8, v48 op_sel_hi:[0,0,0] cbsz:2 blgp:2
	v_mfma_scale_f32_16x16x128_f8f6f4 v[166:169], v[10:15], v[42:47], v[166:169], v16, v48 op_sel_hi:[0,0,0] cbsz:2 blgp:2
	v_mfma_scale_f32_16x16x128_f8f6f4 v[162:165], v[2:7], v[182:187], v[162:165], v8, v188 op_sel_hi:[0,0,0] cbsz:2 blgp:2
	v_mfma_scale_f32_16x16x128_f8f6f4 v[158:161], v[10:15], v[182:187], v[158:161], v16, v188 op_sel_hi:[0,0,0] cbsz:2 blgp:2
	v_mfma_scale_f32_16x16x128_f8f6f4 v[154:157], v[2:7], v[190:195], v[154:157], v8, v196 op_sel_hi:[0,0,0] cbsz:2 blgp:2
	v_mfma_scale_f32_16x16x128_f8f6f4 v[150:153], v[10:15], v[190:195], v[150:153], v16, v196 op_sel_hi:[0,0,0] cbsz:2 blgp:2
	v_mfma_scale_f32_16x16x128_f8f6f4 v[146:149], v[18:23], v[34:39], v[146:149], v24, v40 op_sel_hi:[0,0,0] cbsz:2 blgp:2
	v_mfma_scale_f32_16x16x128_f8f6f4 v[142:145], v[26:31], v[34:39], v[142:145], v32, v40 op_sel_hi:[0,0,0] cbsz:2 blgp:2
	v_mfma_scale_f32_16x16x128_f8f6f4 v[138:141], v[18:23], v[42:47], v[138:141], v24, v48 op_sel_hi:[0,0,0] cbsz:2 blgp:2
	v_mfma_scale_f32_16x16x128_f8f6f4 v[134:137], v[26:31], v[42:47], v[134:137], v32, v48 op_sel_hi:[0,0,0] cbsz:2 blgp:2
	v_mfma_scale_f32_16x16x128_f8f6f4 v[130:133], v[18:23], v[182:187], v[130:133], v24, v188 op_sel_hi:[0,0,0] cbsz:2 blgp:2
	v_mfma_scale_f32_16x16x128_f8f6f4 v[126:129], v[26:31], v[182:187], v[126:129], v32, v188 op_sel_hi:[0,0,0] cbsz:2 blgp:2
	v_mfma_scale_f32_16x16x128_f8f6f4 v[122:125], v[18:23], v[190:195], v[122:125], v24, v196 op_sel_hi:[0,0,0] cbsz:2 blgp:2
	v_mfma_scale_f32_16x16x128_f8f6f4 v[118:121], v[26:31], v[190:195], v[118:121], v32, v196 op_sel_hi:[0,0,0] cbsz:2 blgp:2
	s_setprio 0
	s_barrier
	ds_read_b128 v[34:37], v227 offset:49152
	ds_read_b128 v[38:41], v227 offset:50176
	ds_read_b128 v[42:45], v227 offset:51200
	ds_read_b128 v[46:49], v227 offset:52224
	ds_read_b128 v[182:185], v227 offset:53248
	ds_read_b128 v[186:189], v227 offset:54272
	ds_read_b128 v[190:193], v227 offset:55296
	ds_read_b128 v[194:197], v227 offset:56320
	s_mov_b32 m0, s58
	s_nop 0
	global_load_lds_dwordx4 v219, s[12:13]
	s_nop 0
	s_mov_b32 m0, s59
	s_nop 0
	global_load_lds_dwordx4 v221, s[12:13]
	s_waitcnt vmcnt(4)
	s_waitcnt lgkmcnt(0)
	s_barrier
	s_setprio 1
	s_add_u32 s26, s6, 0x180
	s_addc_u32 s27, s7, 0
	v_mfma_scale_f32_16x16x128_f8f6f4 v[114:117], v[2:7], v[34:39], v[114:117], v8, v40 op_sel_hi:[0,0,0] cbsz:2 blgp:2
	v_mfma_scale_f32_16x16x128_f8f6f4 v[110:113], v[10:15], v[34:39], v[110:113], v16, v40 op_sel_hi:[0,0,0] cbsz:2 blgp:2
	s_mov_b32 m0, s56
	s_nop 0
	global_load_lds_dwordx4 v214, s[26:27]
	v_mfma_scale_f32_16x16x128_f8f6f4 v[106:109], v[2:7], v[42:47], v[106:109], v8, v48 op_sel_hi:[0,0,0] cbsz:2 blgp:2
	v_mfma_scale_f32_16x16x128_f8f6f4 v[102:105], v[10:15], v[42:47], v[102:105], v16, v48 op_sel_hi:[0,0,0] cbsz:2 blgp:2
	s_mov_b32 m0, s57
	s_nop 0
	global_load_lds_dwordx4 v215, s[26:27]
	s_add_u32 s26, s6, 0x40180
	s_addc_u32 s27, s7, 0
	v_mfma_scale_f32_16x16x128_f8f6f4 v[98:101], v[2:7], v[182:187], v[98:101], v8, v188 op_sel_hi:[0,0,0] cbsz:2 blgp:2
	v_mfma_scale_f32_16x16x128_f8f6f4 v[94:97], v[10:15], v[182:187], v[94:97], v16, v188 op_sel_hi:[0,0,0] cbsz:2 blgp:2
	v_mfma_scale_f32_16x16x128_f8f6f4 v[90:93], v[2:7], v[190:195], v[90:93], v8, v196 op_sel_hi:[0,0,0] cbsz:2 blgp:2
	v_mfma_scale_f32_16x16x128_f8f6f4 v[86:89], v[10:15], v[190:195], v[86:89], v16, v196 op_sel_hi:[0,0,0] cbsz:2 blgp:2
	v_mfma_scale_f32_16x16x128_f8f6f4 v[82:85], v[18:23], v[34:39], v[82:85], v24, v40 op_sel_hi:[0,0,0] cbsz:2 blgp:2
	v_mfma_scale_f32_16x16x128_f8f6f4 v[78:81], v[26:31], v[34:39], v[78:81], v32, v40 op_sel_hi:[0,0,0] cbsz:2 blgp:2
	s_mov_b32 m0, s60
	s_nop 0
	global_load_lds_dwordx4 v214, s[26:27]
	v_mfma_scale_f32_16x16x128_f8f6f4 v[74:77], v[18:23], v[42:47], v[74:77], v24, v48 op_sel_hi:[0,0,0] cbsz:2 blgp:2
	v_mfma_scale_f32_16x16x128_f8f6f4 v[70:73], v[26:31], v[42:47], v[70:73], v32, v48 op_sel_hi:[0,0,0] cbsz:2 blgp:2
	s_mov_b32 m0, s61
	s_nop 0
	global_load_lds_dwordx4 v215, s[26:27]
	v_mfma_scale_f32_16x16x128_f8f6f4 v[66:69], v[18:23], v[182:187], v[66:69], v24, v188 op_sel_hi:[0,0,0] cbsz:2 blgp:2
	v_mfma_scale_f32_16x16x128_f8f6f4 v[62:65], v[26:31], v[182:187], v[62:65], v32, v188 op_sel_hi:[0,0,0] cbsz:2 blgp:2
	v_mfma_scale_f32_16x16x128_f8f6f4 v[58:61], v[18:23], v[190:195], v[58:61], v24, v196 op_sel_hi:[0,0,0] cbsz:2 blgp:2
	v_mfma_scale_f32_16x16x128_f8f6f4 v[54:57], v[26:31], v[190:195], v[54:57], v32, v196 op_sel_hi:[0,0,0] cbsz:2 blgp:2
	s_setprio 0
	s_barrier
	s_mov_b32 s28, 2
	s_branch .LBB0_1998

; #define LAS __attribute__((address_space(3)))
; __device__ __forceinline__ unsigned pk4_fp8(float a, float b, float c, float d) { int w = 0; w = __builtin_amdgcn_cvt_pk_fp8_f32(a, b, w, false); w = __builtin_amdgcn_cvt_pk_fp8_f32(c, d, w, true); return (unsigned)w; }
;     __device__ __forceinline__ void operator()(const Acc& acc, const Unit& u, int wr, int wc, int fr, int fq) const {
;         const int row0 = u.pm * 256 + wr * 64 + fr, a0 = u.pn * 128 + wc * 32 + 8 * fq; const LAS float* b1 = bias_lds + (u.ui < 18 ? u.ui : 0) * 256 + 2 * (wc * 32 + 8 * fq); bf16_t* dst = WSP(bf16_t, dst_off);
;         float bg[8], bl[8];
; #pragma unroll
;         for (int q = 0; q < 4; ++q) { const f32x4 t = *(const LAS f32x4*)(b1 + 4 * q); bg[2 * q] = t[0]; bl[2 * q] = t[1] + 1.f; bg[2 * q + 1] = t[2]; bl[2 * q + 1] = t[3] + 1.f; }
; #pragma unroll
;         for (int ai = 0; ai < 2; ++ai)
; #pragma unroll
;             for (int m = 0; m < 4; ++m) { const int row = row0 + ai * 128 + m * 16; float o[8];
; #pragma unroll
;                 for (int j = 0; j < 8; ++j) { float g = acc[ai][0][m][j >> 2][j & 3] * (MOE1_FP6 ? 1.f : W8_INV) + bg[j], l = acc[ai][1][m][j >> 2][j & 3] * (MOE1_FP6 ? 1.f : W8_INV) + bl[j];
;                     g = fminf(g, 7.f); l = fminf(fmaxf(l, -6.f), 8.f);
;                     o[j] = g * __builtin_amdgcn_rcpf(1.f + __builtin_amdgcn_exp2f(-2.4554669595930156f * g)) * l; }
;                 if (MOE_FP8) { u32x2 w; w.x = pk4_fp8(o[0], o[1], o[2], o[3]); w.y = pk4_fp8(o[4], o[5], o[6], o[7]); *(u32x2*)((unsigned char*)dst + (size_t)row * DE + a0) = w; }
.LBB0_2002:
	s_lshl_b32 s2, s50, 8
	s_cmp_lt_i32 s50, 18
	s_cselect_b32 s2, s2, 0
	v_lshl_add_u32 v2, s2, 2, v225
	ds_read_b128 v[14:17], v2
	ds_read_b128 v[10:13], v2 offset:16
	ds_read_b128 v[6:9], v2 offset:32
	ds_read_b128 v[2:5], v2 offset:48
	v_lshl_or_b32 v18, s44, 7, v224
	v_ashrrev_i32_e32 v19, 31, v18
	v_lshl_add_u64 v[20:21], s[14:15], 0, v[18:19]
	v_lshl_add_u32 v22, s43, 8, v223
	v_ashrrev_i32_e32 v23, 31, v22
	v_lshlrev_b64 v[18:19], 11, v[22:23]
	v_lshl_add_u64 v[18:19], v[20:21], 0, v[18:19]
	s_waitcnt lgkmcnt(0)
	v_add_f32_e32 v15, 1.0, v15
	v_add_f32_e32 v17, 1.0, v17
	v_add_f32_e32 v11, 1.0, v11
	v_add_f32_e32 v13, 1.0, v13
	v_add_f32_e32 v7, 1.0, v7
	v_add_f32_e32 v9, 1.0, v9
	v_add_f32_e32 v3, 1.0, v3
	v_add_f32_e32 v5, 1.0, v5
	v_add_f32_e32 v232, v178, v14
	v_add_f32_e32 v233, v179, v16
	v_add_f32_e32 v234, v180, v10
	v_add_f32_e32 v235, v181, v12
	v_add_f32_e32 v236, v174, v6
	v_add_f32_e32 v237, v175, v8
	v_add_f32_e32 v238, v176, v2
	v_add_f32_e32 v239, v177, v4
	v_min_f32_e32 v232, 0x40e00000, v232
	v_min_f32_e32 v233, 0x40e00000, v233
	v_min_f32_e32 v234, 0x40e00000, v234
	v_min_f32_e32 v235, 0x40e00000, v235
	v_min_f32_e32 v236, 0x40e00000, v236
	v_min_f32_e32 v237, 0x40e00000, v237
	v_min_f32_e32 v238, 0x40e00000, v238
	v_min_f32_e32 v239, 0x40e00000, v239
	v_mul_f32_e32 v243, 0xc01d265f, v232
	v_mul_f32_e32 v244, 0xc01d265f, v233
	v_mul_f32_e32 v245, 0xc01d265f, v234
	v_mul_f32_e32 v246, 0xc01d265f, v235
	v_mul_f32_e32 v247, 0xc01d265f, v236
	v_mul_f32_e32 v248, 0xc01d265f, v237
	v_mul_f32_e32 v249, 0xc01d265f, v238
	v_mul_f32_e32 v250, 0xc01d265f, v239
	v_exp_f32_e32 v243, v243
	v_exp_f32_e32 v244, v244
	v_exp_f32_e32 v245, v245
	v_exp_f32_e32 v246, v246
	v_exp_f32_e32 v247, v247
	v_exp_f32_e32 v248, v248
	v_exp_f32_e32 v249, v249
	v_exp_f32_e32 v250, v250
	v_add_f32_e32 v202, v146, v15
	v_add_f32_e32 v203, v147, v17
	v_add_f32_e32 v204, v148, v11
	v_add_f32_e32 v205, v149, v13
	v_add_f32_e32 v206, v142, v7
	v_add_f32_e32 v207, v143, v9
	v_add_f32_e32 v208, v144, v3
	v_add_f32_e32 v209, v145, v5
	v_med3_f32 v202, v202, s86, v228
	v_med3_f32 v203, v203, s86, v228
	v_med3_f32 v204, v204, s86, v228
	v_med3_f32 v205, v205, s86, v228
	v_med3_f32 v206, v206, s86, v228
	v_med3_f32 v207, v207, s86, v228
	v_med3_f32 v208, v208, s86, v228
	v_med3_f32 v209, v209, s86, v228
	v_add_f32_e32 v243, 1.0, v243
	v_add_f32_e32 v244, 1.0, v244
	v_add_f32_e32 v245, 1.0, v245
	v_add_f32_e32 v246, 1.0, v246
	v_add_f32_e32 v247, 1.0, v247
	v_add_f32_e32 v248, 1.0, v248
	v_add_f32_e32 v249, 1.0, v249
	v_add_f32_e32 v250, 1.0, v250
	v_rcp_f32_e32 v243, v243
	v_rcp_f32_e32 v244, v244
	v_rcp_f32_e32 v245, v245
	v_rcp_f32_e32 v246, v246
	v_rcp_f32_e32 v247, v247
	v_rcp_f32_e32 v248, v248
	v_rcp_f32_e32 v249, v249
	v_rcp_f32_e32 v250, v250
	v_mul_f32_e32 v232, v232, v243
	v_mul_f32_e32 v233, v233, v244
	v_mul_f32_e32 v234, v234, v245
	v_mul_f32_e32 v235, v235, v246
	v_mul_f32_e32 v236, v236, v247
	v_mul_f32_e32 v237, v237, v248
	v_mul_f32_e32 v238, v238, v249
	v_mul_f32_e32 v239, v239, v250
	v_mul_f32_e32 v232, v202, v232
	v_mul_f32_e32 v233, v203, v233
	v_mul_f32_e32 v234, v204, v234
	v_mul_f32_e32 v235, v205, v235
	v_mul_f32_e32 v236, v206, v236
	v_mul_f32_e32 v237, v207, v237
	v_mul_f32_e32 v238, v208, v238
	v_mul_f32_e32 v239, v209, v239
	v_mov_b32_e32 v210, 0
	v_mov_b32_e32 v211, 0
	v_cvt_pk_fp8_f32 v210, v232, v233
	v_cvt_pk_fp8_f32 v211, v236, v237
	v_cvt_pk_fp8_f32 v210, v234, v235 op_sel:[0,0,1]
	v_cvt_pk_fp8_f32 v211, v238, v239 op_sel:[0,0,1]
	s_nop 0
	global_store_dwordx2 v[18:19], v[210:211], off
	v_add_f32_e32 v232, v170, v14
	v_add_f32_e32 v233, v171, v16
	v_add_f32_e32 v234, v172, v10
	v_add_f32_e32 v235, v173, v12
	v_add_f32_e32 v236, v166, v6
	v_add_f32_e32 v237, v167, v8
	v_add_f32_e32 v238, v168, v2
	v_add_f32_e32 v239, v169, v4
	v_min_f32_e32 v232, 0x40e00000, v232
	v_min_f32_e32 v233, 0x40e00000, v233
	v_min_f32_e32 v234, 0x40e00000, v234
	v_min_f32_e32 v235, 0x40e00000, v235
	v_min_f32_e32 v236, 0x40e00000, v236
	v_min_f32_e32 v237, 0x40e00000, v237
	v_min_f32_e32 v238, 0x40e00000, v238
	v_min_f32_e32 v239, 0x40e00000, v239
	v_mul_f32_e32 v243, 0xc01d265f, v232
	v_mul_f32_e32 v244, 0xc01d265f, v233
	v_mul_f32_e32 v245, 0xc01d265f, v234
	v_mul_f32_e32 v246, 0xc01d265f, v235
	v_mul_f32_e32 v247, 0xc01d265f, v236
	v_mul_f32_e32 v248, 0xc01d265f, v237
	v_mul_f32_e32 v249, 0xc01d265f, v238
	v_mul_f32_e32 v250, 0xc01d265f, v239
	v_exp_f32_e32 v243, v243
	v_exp_f32_e32 v244, v244
	v_exp_f32_e32 v245, v245
	v_exp_f32_e32 v246, v246
	v_exp_f32_e32 v247, v247
	v_exp_f32_e32 v248, v248
	v_exp_f32_e32 v249, v249
	v_exp_f32_e32 v250, v250
	v_add_f32_e32 v202, v138, v15
	v_add_f32_e32 v203, v139, v17
	v_add_f32_e32 v204, v140, v11
	v_add_f32_e32 v205, v141, v13
	v_add_f32_e32 v206, v134, v7
	v_add_f32_e32 v207, v135, v9
	v_add_f32_e32 v208, v136, v3
	v_add_f32_e32 v209, v137, v5
	v_med3_f32 v202, v202, s86, v228
	v_med3_f32 v203, v203, s86, v228
	v_med3_f32 v204, v204, s86, v228
	v_med3_f32 v205, v205, s86, v228
	v_med3_f32 v206, v206, s86, v228
	v_med3_f32 v207, v207, s86, v228
	v_med3_f32 v208, v208, s86, v228
	v_med3_f32 v209, v209, s86, v228
	v_add_f32_e32 v243, 1.0, v243
	v_add_f32_e32 v244, 1.0, v244
	v_add_f32_e32 v245, 1.0, v245
	v_add_f32_e32 v246, 1.0, v246
	v_add_f32_e32 v247, 1.0, v247
	v_add_f32_e32 v248, 1.0, v248
	v_add_f32_e32 v249, 1.0, v249
	v_add_f32_e32 v250, 1.0, v250
	v_rcp_f32_e32 v243, v243
	v_rcp_f32_e32 v244, v244
	v_rcp_f32_e32 v245, v245
	v_rcp_f32_e32 v246, v246
	v_rcp_f32_e32 v247, v247
	v_rcp_f32_e32 v248, v248
	v_rcp_f32_e32 v249, v249
	v_rcp_f32_e32 v250, v250
	v_mul_f32_e32 v232, v232, v243
; __device__ __forceinline__ unsigned pk4_fp8(float a, float b, float c, float d) { int w = 0; w = __builtin_amdgcn_cvt_pk_fp8_f32(a, b, w, false); w = __builtin_amdgcn_cvt_pk_fp8_f32(c, d, w, true); return (unsigned)w; }
;     __device__ __forceinline__ void operator()(const Acc& acc, const Unit& u, int wr, int wc, int fr, int fq) const {
;     ...
;             for (int m = 0; m < 4; ++m) { const int row = row0 + ai * 128 + m * 16; float o[8];
; #pragma unroll
;                 for (int j = 0; j < 8; ++j) { float g = acc[ai][0][m][j >> 2][j & 3] * (MOE1_FP6 ? 1.f : W8_INV) + bg[j], l = acc[ai][1][m][j >> 2][j & 3] * (MOE1_FP6 ? 1.f : W8_INV) + bl[j];
;                     g = fminf(g, 7.f); l = fminf(fmaxf(l, -6.f), 8.f);
;                     o[j] = g * __builtin_amdgcn_rcpf(1.f + __builtin_amdgcn_exp2f(-2.4554669595930156f * g)) * l; }
;                 if (MOE_FP8) { u32x2 w; w.x = pk4_fp8(o[0], o[1], o[2], o[3]); w.y = pk4_fp8(o[4], o[5], o[6], o[7]); *(u32x2*)((unsigned char*)dst + (size_t)row * DE + a0) = w; }
	v_mul_f32_e32 v233, v233, v244
	v_mul_f32_e32 v234, v234, v245
	v_mul_f32_e32 v235, v235, v246
	v_mul_f32_e32 v236, v236, v247
	v_mul_f32_e32 v237, v237, v248
	v_mul_f32_e32 v238, v238, v249
	v_mul_f32_e32 v239, v239, v250
	v_mul_f32_e32 v232, v202, v232
	v_mul_f32_e32 v233, v203, v233
	v_mul_f32_e32 v234, v204, v234
	v_mul_f32_e32 v235, v205, v235
	v_mul_f32_e32 v236, v206, v236
	v_mul_f32_e32 v237, v207, v237
	v_mul_f32_e32 v238, v208, v238
	v_mul_f32_e32 v239, v209, v239
	v_mov_b32_e32 v212, 0
	v_mov_b32_e32 v213, 0
	v_cvt_pk_fp8_f32 v212, v232, v233
	v_cvt_pk_fp8_f32 v213, v236, v237
	v_cvt_pk_fp8_f32 v212, v234, v235 op_sel:[0,0,1]
	v_cvt_pk_fp8_f32 v213, v238, v239 op_sel:[0,0,1]
	v_add_co_u32_e32 v24, vcc, 0x8000, v18
	s_nop 1
	v_addc_co_u32_e32 v25, vcc, 0, v19, vcc
	global_store_dwordx2 v[24:25], v[212:213], off
	v_add_f32_e32 v232, v162, v14
	v_add_f32_e32 v233, v163, v16
	v_add_f32_e32 v234, v164, v10
	v_add_f32_e32 v235, v165, v12
	v_add_f32_e32 v236, v158, v6
	v_add_f32_e32 v237, v159, v8
	v_add_f32_e32 v238, v160, v2
	v_add_f32_e32 v239, v161, v4
	v_min_f32_e32 v232, 0x40e00000, v232
	v_min_f32_e32 v233, 0x40e00000, v233
	v_min_f32_e32 v234, 0x40e00000, v234
	v_min_f32_e32 v235, 0x40e00000, v235
	v_min_f32_e32 v236, 0x40e00000, v236
	v_min_f32_e32 v237, 0x40e00000, v237
	v_min_f32_e32 v238, 0x40e00000, v238
	v_min_f32_e32 v239, 0x40e00000, v239
	v_mul_f32_e32 v243, 0xc01d265f, v232
	v_mul_f32_e32 v244, 0xc01d265f, v233
	v_mul_f32_e32 v245, 0xc01d265f, v234
	v_mul_f32_e32 v246, 0xc01d265f, v235
	v_mul_f32_e32 v247, 0xc01d265f, v236
	v_mul_f32_e32 v248, 0xc01d265f, v237
	v_mul_f32_e32 v249, 0xc01d265f, v238
	v_mul_f32_e32 v250, 0xc01d265f, v239
	v_exp_f32_e32 v243, v243
	v_exp_f32_e32 v244, v244
	v_exp_f32_e32 v245, v245
	v_exp_f32_e32 v246, v246
	v_exp_f32_e32 v247, v247
	v_exp_f32_e32 v248, v248
	v_exp_f32_e32 v249, v249
	v_exp_f32_e32 v250, v250
	v_add_f32_e32 v202, v130, v15
	v_add_f32_e32 v203, v131, v17
	v_add_f32_e32 v204, v132, v11
	v_add_f32_e32 v205, v133, v13
	v_add_f32_e32 v206, v126, v7
	v_add_f32_e32 v207, v127, v9
	v_add_f32_e32 v208, v128, v3
	v_add_f32_e32 v209, v129, v5
	v_med3_f32 v202, v202, s86, v228
	v_med3_f32 v203, v203, s86, v228
	v_med3_f32 v204, v204, s86, v228
	v_med3_f32 v205, v205, s86, v228
	v_med3_f32 v206, v206, s86, v228
	v_med3_f32 v207, v207, s86, v228
	v_med3_f32 v208, v208, s86, v228
	v_med3_f32 v209, v209, s86, v228
	v_add_f32_e32 v243, 1.0, v243
	v_add_f32_e32 v244, 1.0, v244
	v_add_f32_e32 v245, 1.0, v245
	v_add_f32_e32 v246, 1.0, v246
	v_add_f32_e32 v247, 1.0, v247
	v_add_f32_e32 v248, 1.0, v248
	v_add_f32_e32 v249, 1.0, v249
	v_add_f32_e32 v250, 1.0, v250
	v_rcp_f32_e32 v243, v243
	v_rcp_f32_e32 v244, v244
	v_rcp_f32_e32 v245, v245
	v_rcp_f32_e32 v246, v246
	v_rcp_f32_e32 v247, v247
	v_rcp_f32_e32 v248, v248
	v_rcp_f32_e32 v249, v249
	v_rcp_f32_e32 v250, v250
	v_mul_f32_e32 v232, v232, v243
	v_mul_f32_e32 v233, v233, v244
	v_mul_f32_e32 v234, v234, v245
	v_mul_f32_e32 v235, v235, v246
	v_mul_f32_e32 v236, v236, v247
	v_mul_f32_e32 v237, v237, v248
	v_mul_f32_e32 v238, v238, v249
	v_mul_f32_e32 v239, v239, v250
	v_mul_f32_e32 v232, v202, v232
	v_mul_f32_e32 v233, v203, v233
	v_mul_f32_e32 v234, v204, v234
	v_mul_f32_e32 v235, v205, v235
	v_mul_f32_e32 v236, v206, v236
	v_mul_f32_e32 v237, v207, v237
	v_mul_f32_e32 v238, v208, v238
	v_mul_f32_e32 v239, v209, v239
	v_mov_b32_e32 v210, 0
	v_mov_b32_e32 v211, 0
	v_cvt_pk_fp8_f32 v210, v232, v233
	v_cvt_pk_fp8_f32 v211, v236, v237
	v_cvt_pk_fp8_f32 v210, v234, v235 op_sel:[0,0,1]
	v_cvt_pk_fp8_f32 v211, v238, v239 op_sel:[0,0,1]
	v_add_co_u32_e32 v24, vcc, 0x10000, v18
	s_nop 1
	v_addc_co_u32_e32 v25, vcc, 0, v19, vcc
	global_store_dwordx2 v[24:25], v[210:211], off
	v_add_f32_e32 v232, v154, v14
	v_add_f32_e32 v233, v155, v16
	v_add_f32_e32 v234, v156, v10
	v_add_f32_e32 v235, v157, v12
	v_add_f32_e32 v236, v150, v6
	v_add_f32_e32 v237, v151, v8
	v_add_f32_e32 v238, v152, v2
	v_add_f32_e32 v239, v153, v4
	v_min_f32_e32 v232, 0x40e00000, v232
	v_min_f32_e32 v233, 0x40e00000, v233
	v_min_f32_e32 v234, 0x40e00000, v234
	v_min_f32_e32 v235, 0x40e00000, v235
	v_min_f32_e32 v236, 0x40e00000, v236
	v_min_f32_e32 v237, 0x40e00000, v237
	v_min_f32_e32 v238, 0x40e00000, v238
	v_min_f32_e32 v239, 0x40e00000, v239
	v_mul_f32_e32 v243, 0xc01d265f, v232
	v_mul_f32_e32 v244, 0xc01d265f, v233
	v_mul_f32_e32 v245, 0xc01d265f, v234
	v_mul_f32_e32 v246, 0xc01d265f, v235
	v_mul_f32_e32 v247, 0xc01d265f, v236
	v_mul_f32_e32 v248, 0xc01d265f, v237
	v_mul_f32_e32 v249, 0xc01d265f, v238
	v_mul_f32_e32 v250, 0xc01d265f, v239
	v_exp_f32_e32 v243, v243
	v_exp_f32_e32 v244, v244
	v_exp_f32_e32 v245, v245
	v_exp_f32_e32 v246, v246
	v_exp_f32_e32 v247, v247
	v_exp_f32_e32 v248, v248
	v_exp_f32_e32 v249, v249
	v_exp_f32_e32 v250, v250
	v_add_f32_e32 v202, v122, v15
	v_add_f32_e32 v203, v123, v17
	v_add_f32_e32 v204, v124, v11
	v_add_f32_e32 v205, v125, v13
	v_add_f32_e32 v206, v118, v7
	v_add_f32_e32 v207, v119, v9
	v_add_f32_e32 v208, v120, v3
	v_add_f32_e32 v209, v121, v5
	v_med3_f32 v202, v202, s86, v228
	v_med3_f32 v203, v203, s86, v228
	v_med3_f32 v204, v204, s86, v228
	v_med3_f32 v205, v205, s86, v228
	v_med3_f32 v206, v206, s86, v228
	v_med3_f32 v207, v207, s86, v228
	v_med3_f32 v208, v208, s86, v228
	v_med3_f32 v209, v209, s86, v228
	v_add_f32_e32 v243, 1.0, v243
	v_add_f32_e32 v244, 1.0, v244
	v_add_f32_e32 v245, 1.0, v245
	v_add_f32_e32 v246, 1.0, v246
	v_add_f32_e32 v247, 1.0, v247
	v_add_f32_e32 v248, 1.0, v248
	v_add_f32_e32 v249, 1.0, v249
	v_add_f32_e32 v250, 1.0, v250
	v_rcp_f32_e32 v243, v243
	v_rcp_f32_e32 v244, v244
	v_rcp_f32_e32 v245, v245
; __device__ __forceinline__ unsigned pk4_fp8(float a, float b, float c, float d) { int w = 0; w = __builtin_amdgcn_cvt_pk_fp8_f32(a, b, w, false); w = __builtin_amdgcn_cvt_pk_fp8_f32(c, d, w, true); return (unsigned)w; }
;     __device__ __forceinline__ void operator()(const Acc& acc, const Unit& u, int wr, int wc, int fr, int fq) const {
;     ...
;             for (int m = 0; m < 4; ++m) { const int row = row0 + ai * 128 + m * 16; float o[8];
; #pragma unroll
;                 for (int j = 0; j < 8; ++j) { float g = acc[ai][0][m][j >> 2][j & 3] * (MOE1_FP6 ? 1.f : W8_INV) + bg[j], l = acc[ai][1][m][j >> 2][j & 3] * (MOE1_FP6 ? 1.f : W8_INV) + bl[j];
;                     g = fminf(g, 7.f); l = fminf(fmaxf(l, -6.f), 8.f);
;                     o[j] = g * __builtin_amdgcn_rcpf(1.f + __builtin_amdgcn_exp2f(-2.4554669595930156f * g)) * l; }
;                 if (MOE_FP8) { u32x2 w; w.x = pk4_fp8(o[0], o[1], o[2], o[3]); w.y = pk4_fp8(o[4], o[5], o[6], o[7]); *(u32x2*)((unsigned char*)dst + (size_t)row * DE + a0) = w; }
	v_rcp_f32_e32 v246, v246
	v_rcp_f32_e32 v247, v247
	v_rcp_f32_e32 v248, v248
	v_rcp_f32_e32 v249, v249
	v_rcp_f32_e32 v250, v250
	v_mul_f32_e32 v232, v232, v243
	v_mul_f32_e32 v233, v233, v244
	v_mul_f32_e32 v234, v234, v245
	v_mul_f32_e32 v235, v235, v246
	v_mul_f32_e32 v236, v236, v247
	v_mul_f32_e32 v237, v237, v248
	v_mul_f32_e32 v238, v238, v249
	v_mul_f32_e32 v239, v239, v250
	v_mul_f32_e32 v232, v202, v232
	v_mul_f32_e32 v233, v203, v233
	v_mul_f32_e32 v234, v204, v234
	v_mul_f32_e32 v235, v205, v235
	v_mul_f32_e32 v236, v206, v236
	v_mul_f32_e32 v237, v207, v237
	v_mul_f32_e32 v238, v208, v238
	v_mul_f32_e32 v239, v209, v239
	v_mov_b32_e32 v212, 0
	v_mov_b32_e32 v213, 0
	v_cvt_pk_fp8_f32 v212, v232, v233
	v_cvt_pk_fp8_f32 v213, v236, v237
	v_cvt_pk_fp8_f32 v212, v234, v235 op_sel:[0,0,1]
	v_cvt_pk_fp8_f32 v213, v238, v239 op_sel:[0,0,1]
	v_add_co_u32_e32 v24, vcc, 0x18000, v18
	s_nop 1
	v_addc_co_u32_e32 v25, vcc, 0, v19, vcc
	global_store_dwordx2 v[24:25], v[212:213], off
	v_add_f32_e32 v232, v114, v14
	v_add_f32_e32 v233, v115, v16
	v_add_f32_e32 v234, v116, v10
	v_add_f32_e32 v235, v117, v12
	v_add_f32_e32 v236, v110, v6
	v_add_f32_e32 v237, v111, v8
	v_add_f32_e32 v238, v112, v2
	v_add_f32_e32 v239, v113, v4
	v_min_f32_e32 v232, 0x40e00000, v232
	v_min_f32_e32 v233, 0x40e00000, v233
	v_min_f32_e32 v234, 0x40e00000, v234
	v_min_f32_e32 v235, 0x40e00000, v235
	v_min_f32_e32 v236, 0x40e00000, v236
	v_min_f32_e32 v237, 0x40e00000, v237
	v_min_f32_e32 v238, 0x40e00000, v238
	v_min_f32_e32 v239, 0x40e00000, v239
	v_mul_f32_e32 v243, 0xc01d265f, v232
	v_mul_f32_e32 v244, 0xc01d265f, v233
	v_mul_f32_e32 v245, 0xc01d265f, v234
	v_mul_f32_e32 v246, 0xc01d265f, v235
	v_mul_f32_e32 v247, 0xc01d265f, v236
	v_mul_f32_e32 v248, 0xc01d265f, v237
	v_mul_f32_e32 v249, 0xc01d265f, v238
	v_mul_f32_e32 v250, 0xc01d265f, v239
	v_exp_f32_e32 v243, v243
	v_exp_f32_e32 v244, v244
	v_exp_f32_e32 v245, v245
	v_exp_f32_e32 v246, v246
	v_exp_f32_e32 v247, v247
	v_exp_f32_e32 v248, v248
	v_exp_f32_e32 v249, v249
	v_exp_f32_e32 v250, v250
	v_add_f32_e32 v202, v82, v15
	v_add_f32_e32 v203, v83, v17
	v_add_f32_e32 v204, v84, v11
	v_add_f32_e32 v205, v85, v13
	v_add_f32_e32 v206, v78, v7
	v_add_f32_e32 v207, v79, v9
	v_add_f32_e32 v208, v80, v3
	v_add_f32_e32 v209, v81, v5
	v_med3_f32 v202, v202, s86, v228
	v_med3_f32 v203, v203, s86, v228
	v_med3_f32 v204, v204, s86, v228
	v_med3_f32 v205, v205, s86, v228
	v_med3_f32 v206, v206, s86, v228
	v_med3_f32 v207, v207, s86, v228
	v_med3_f32 v208, v208, s86, v228
	v_med3_f32 v209, v209, s86, v228
	v_add_f32_e32 v243, 1.0, v243
	v_add_f32_e32 v244, 1.0, v244
	v_add_f32_e32 v245, 1.0, v245
	v_add_f32_e32 v246, 1.0, v246
	v_add_f32_e32 v247, 1.0, v247
	v_add_f32_e32 v248, 1.0, v248
	v_add_f32_e32 v249, 1.0, v249
	v_add_f32_e32 v250, 1.0, v250
	v_rcp_f32_e32 v243, v243
	v_rcp_f32_e32 v244, v244
	v_rcp_f32_e32 v245, v245
	v_rcp_f32_e32 v246, v246
	v_rcp_f32_e32 v247, v247
	v_rcp_f32_e32 v248, v248
	v_rcp_f32_e32 v249, v249
	v_rcp_f32_e32 v250, v250
	v_mul_f32_e32 v232, v232, v243
	v_mul_f32_e32 v233, v233, v244
	v_mul_f32_e32 v234, v234, v245
	v_mul_f32_e32 v235, v235, v246
	v_mul_f32_e32 v236, v236, v247
	v_mul_f32_e32 v237, v237, v248
	v_mul_f32_e32 v238, v238, v249
	v_mul_f32_e32 v239, v239, v250
	v_mul_f32_e32 v232, v202, v232
	v_mul_f32_e32 v233, v203, v233
	v_mul_f32_e32 v234, v204, v234
	v_mul_f32_e32 v235, v205, v235
	v_mul_f32_e32 v236, v206, v236
	v_mul_f32_e32 v237, v207, v237
	v_mul_f32_e32 v238, v208, v238
	v_mul_f32_e32 v239, v209, v239
	v_mov_b32_e32 v210, 0
	v_mov_b32_e32 v211, 0
	v_cvt_pk_fp8_f32 v210, v232, v233
	v_cvt_pk_fp8_f32 v211, v236, v237
	v_cvt_pk_fp8_f32 v210, v234, v235 op_sel:[0,0,1]
	v_cvt_pk_fp8_f32 v211, v238, v239 op_sel:[0,0,1]
	v_add_co_u32_e32 v24, vcc, 0x40000, v18
	s_nop 1
	v_addc_co_u32_e32 v25, vcc, 0, v19, vcc
	global_store_dwordx2 v[24:25], v[210:211], off
	v_add_f32_e32 v232, v106, v14
	v_add_f32_e32 v233, v107, v16
	v_add_f32_e32 v234, v108, v10
	v_add_f32_e32 v235, v109, v12
	v_add_f32_e32 v236, v102, v6
	v_add_f32_e32 v237, v103, v8
	v_add_f32_e32 v238, v104, v2
	v_add_f32_e32 v239, v105, v4
	v_min_f32_e32 v232, 0x40e00000, v232
	v_min_f32_e32 v233, 0x40e00000, v233
	v_min_f32_e32 v234, 0x40e00000, v234
	v_min_f32_e32 v235, 0x40e00000, v235
	v_min_f32_e32 v236, 0x40e00000, v236
	v_min_f32_e32 v237, 0x40e00000, v237
	v_min_f32_e32 v238, 0x40e00000, v238
	v_min_f32_e32 v239, 0x40e00000, v239
	v_mul_f32_e32 v243, 0xc01d265f, v232
	v_mul_f32_e32 v244, 0xc01d265f, v233
	v_mul_f32_e32 v245, 0xc01d265f, v234
	v_mul_f32_e32 v246, 0xc01d265f, v235
	v_mul_f32_e32 v247, 0xc01d265f, v236
	v_mul_f32_e32 v248, 0xc01d265f, v237
	v_mul_f32_e32 v249, 0xc01d265f, v238
	v_mul_f32_e32 v250, 0xc01d265f, v239
	v_exp_f32_e32 v243, v243
	v_exp_f32_e32 v244, v244
	v_exp_f32_e32 v245, v245
	v_exp_f32_e32 v246, v246
	v_exp_f32_e32 v247, v247
	v_exp_f32_e32 v248, v248
	v_exp_f32_e32 v249, v249
	v_exp_f32_e32 v250, v250
	v_add_f32_e32 v202, v74, v15
	v_add_f32_e32 v203, v75, v17
	v_add_f32_e32 v204, v76, v11
	v_add_f32_e32 v205, v77, v13
	v_add_f32_e32 v206, v70, v7
	v_add_f32_e32 v207, v71, v9
	v_add_f32_e32 v208, v72, v3
	v_add_f32_e32 v209, v73, v5
	v_med3_f32 v202, v202, s86, v228
	v_med3_f32 v203, v203, s86, v228
	v_med3_f32 v204, v204, s86, v228
	v_med3_f32 v205, v205, s86, v228
	v_med3_f32 v206, v206, s86, v228
	v_med3_f32 v207, v207, s86, v228
	v_med3_f32 v208, v208, s86, v228
	v_med3_f32 v209, v209, s86, v228
	v_add_f32_e32 v243, 1.0, v243
	v_add_f32_e32 v244, 1.0, v244
	v_add_f32_e32 v245, 1.0, v245
	v_add_f32_e32 v246, 1.0, v246
	v_add_f32_e32 v247, 1.0, v247
	v_add_f32_e32 v248, 1.0, v248
; __device__ __forceinline__ unsigned pk2(float a, float b) { f32x2_t v = {a, b}; bf16x2_t r = __builtin_convertvector(v, bf16x2_t); return __builtin_bit_cast(unsigned, r); }
; __device__ __forceinline__ unsigned pk4_fp8(float a, float b, float c, float d) { int w = 0; w = __builtin_amdgcn_cvt_pk_fp8_f32(a, b, w, false); w = __builtin_amdgcn_cvt_pk_fp8_f32(c, d, w, true); return (unsigned)w; }
;     __device__ __forceinline__ void operator()(const Acc& acc, const Unit& u, int wr, int wc, int fr, int fq) const {
;     ...
;             for (int m = 0; m < 4; ++m) { const int row = row0 + ai * 128 + m * 16; float o[8];
; #pragma unroll
;                 for (int j = 0; j < 8; ++j) { float g = acc[ai][0][m][j >> 2][j & 3] * (MOE1_FP6 ? 1.f : W8_INV) + bg[j], l = acc[ai][1][m][j >> 2][j & 3] * (MOE1_FP6 ? 1.f : W8_INV) + bl[j];
;                     g = fminf(g, 7.f); l = fminf(fmaxf(l, -6.f), 8.f);
;                     o[j] = g * __builtin_amdgcn_rcpf(1.f + __builtin_amdgcn_exp2f(-2.4554669595930156f * g)) * l; }
;                 if (MOE_FP8) { u32x2 w; w.x = pk4_fp8(o[0], o[1], o[2], o[3]); w.y = pk4_fp8(o[4], o[5], o[6], o[7]); *(u32x2*)((unsigned char*)dst + (size_t)row * DE + a0) = w; }
;                 else { u32x4 w; w.x = pk2(o[0], o[1]); w.y = pk2(o[2], o[3]); w.z = pk2(o[4], o[5]); w.w = pk2(o[6], o[7]);
;                 *(u32x4*)(dst + (size_t)row * DE + a0) = w; } }
	v_add_f32_e32 v249, 1.0, v249
	v_add_f32_e32 v250, 1.0, v250
	v_rcp_f32_e32 v243, v243
	v_rcp_f32_e32 v244, v244
	v_rcp_f32_e32 v245, v245
	v_rcp_f32_e32 v246, v246
	v_rcp_f32_e32 v247, v247
	v_rcp_f32_e32 v248, v248
	v_rcp_f32_e32 v249, v249
	v_rcp_f32_e32 v250, v250
	v_mul_f32_e32 v232, v232, v243
	v_mul_f32_e32 v233, v233, v244
	v_mul_f32_e32 v234, v234, v245
	v_mul_f32_e32 v235, v235, v246
	v_mul_f32_e32 v236, v236, v247
	v_mul_f32_e32 v237, v237, v248
	v_mul_f32_e32 v238, v238, v249
	v_mul_f32_e32 v239, v239, v250
	v_mul_f32_e32 v232, v202, v232
	v_mul_f32_e32 v233, v203, v233
	v_mul_f32_e32 v234, v204, v234
	v_mul_f32_e32 v235, v205, v235
	v_mul_f32_e32 v236, v206, v236
	v_mul_f32_e32 v237, v207, v237
	v_mul_f32_e32 v238, v208, v238
	v_mul_f32_e32 v239, v209, v239
	v_mov_b32_e32 v212, 0
	v_mov_b32_e32 v213, 0
	v_cvt_pk_fp8_f32 v212, v232, v233
	v_cvt_pk_fp8_f32 v213, v236, v237
	v_cvt_pk_fp8_f32 v212, v234, v235 op_sel:[0,0,1]
	v_cvt_pk_fp8_f32 v213, v238, v239 op_sel:[0,0,1]
	v_add_co_u32_e32 v24, vcc, 0x48000, v18
	s_nop 1
	v_addc_co_u32_e32 v25, vcc, 0, v19, vcc
	global_store_dwordx2 v[24:25], v[212:213], off
	v_add_f32_e32 v232, v98, v14
	v_add_f32_e32 v233, v99, v16
	v_add_f32_e32 v234, v100, v10
	v_add_f32_e32 v235, v101, v12
	v_add_f32_e32 v236, v94, v6
	v_add_f32_e32 v237, v95, v8
	v_add_f32_e32 v238, v96, v2
	v_add_f32_e32 v239, v97, v4
	v_min_f32_e32 v232, 0x40e00000, v232
	v_min_f32_e32 v233, 0x40e00000, v233
	v_min_f32_e32 v234, 0x40e00000, v234
	v_min_f32_e32 v235, 0x40e00000, v235
	v_min_f32_e32 v236, 0x40e00000, v236
	v_min_f32_e32 v237, 0x40e00000, v237
	v_min_f32_e32 v238, 0x40e00000, v238
	v_min_f32_e32 v239, 0x40e00000, v239
	v_mul_f32_e32 v243, 0xc01d265f, v232
	v_mul_f32_e32 v244, 0xc01d265f, v233
	v_mul_f32_e32 v245, 0xc01d265f, v234
	v_mul_f32_e32 v246, 0xc01d265f, v235
	v_mul_f32_e32 v247, 0xc01d265f, v236
	v_mul_f32_e32 v248, 0xc01d265f, v237
	v_mul_f32_e32 v249, 0xc01d265f, v238
	v_mul_f32_e32 v250, 0xc01d265f, v239
	v_exp_f32_e32 v243, v243
	v_exp_f32_e32 v244, v244
	v_exp_f32_e32 v245, v245
	v_exp_f32_e32 v246, v246
	v_exp_f32_e32 v247, v247
	v_exp_f32_e32 v248, v248
	v_exp_f32_e32 v249, v249
	v_exp_f32_e32 v250, v250
	v_add_f32_e32 v202, v66, v15
	v_add_f32_e32 v203, v67, v17
	v_add_f32_e32 v204, v68, v11
	v_add_f32_e32 v205, v69, v13
	v_add_f32_e32 v206, v62, v7
	v_add_f32_e32 v207, v63, v9
	v_add_f32_e32 v208, v64, v3
	v_add_f32_e32 v209, v65, v5
	v_med3_f32 v202, v202, s86, v228
	v_med3_f32 v203, v203, s86, v228
	v_med3_f32 v204, v204, s86, v228
	v_med3_f32 v205, v205, s86, v228
	v_med3_f32 v206, v206, s86, v228
	v_med3_f32 v207, v207, s86, v228
	v_med3_f32 v208, v208, s86, v228
	v_med3_f32 v209, v209, s86, v228
	v_add_f32_e32 v243, 1.0, v243
	v_add_f32_e32 v244, 1.0, v244
	v_add_f32_e32 v245, 1.0, v245
	v_add_f32_e32 v246, 1.0, v246
	v_add_f32_e32 v247, 1.0, v247
	v_add_f32_e32 v248, 1.0, v248
	v_add_f32_e32 v249, 1.0, v249
	v_add_f32_e32 v250, 1.0, v250
	v_rcp_f32_e32 v243, v243
	v_rcp_f32_e32 v244, v244
	v_rcp_f32_e32 v245, v245
	v_rcp_f32_e32 v246, v246
	v_rcp_f32_e32 v247, v247
	v_rcp_f32_e32 v248, v248
	v_rcp_f32_e32 v249, v249
	v_rcp_f32_e32 v250, v250
	v_mul_f32_e32 v232, v232, v243
	v_mul_f32_e32 v233, v233, v244
	v_mul_f32_e32 v234, v234, v245
	v_mul_f32_e32 v235, v235, v246
	v_mul_f32_e32 v236, v236, v247
	v_mul_f32_e32 v237, v237, v248
	v_mul_f32_e32 v238, v238, v249
	v_mul_f32_e32 v239, v239, v250
	v_mul_f32_e32 v232, v202, v232
	v_mul_f32_e32 v233, v203, v233
	v_mul_f32_e32 v234, v204, v234
	v_mul_f32_e32 v235, v205, v235
	v_mul_f32_e32 v236, v206, v236
	v_mul_f32_e32 v237, v207, v237
	v_mul_f32_e32 v238, v208, v238
	v_mul_f32_e32 v239, v209, v239
	v_mov_b32_e32 v210, 0
	v_mov_b32_e32 v211, 0
	v_cvt_pk_fp8_f32 v210, v232, v233
	v_cvt_pk_fp8_f32 v211, v236, v237
	v_cvt_pk_fp8_f32 v210, v234, v235 op_sel:[0,0,1]
	v_cvt_pk_fp8_f32 v211, v238, v239 op_sel:[0,0,1]
	v_add_co_u32_e32 v24, vcc, 0x50000, v18
	s_nop 1
	v_addc_co_u32_e32 v25, vcc, 0, v19, vcc
	global_store_dwordx2 v[24:25], v[210:211], off
	v_add_f32_e32 v232, v90, v14
	v_add_f32_e32 v233, v91, v16
	v_add_f32_e32 v234, v92, v10
	v_add_f32_e32 v235, v93, v12
	v_add_f32_e32 v236, v86, v6
	v_add_f32_e32 v237, v87, v8
	v_add_f32_e32 v238, v88, v2
	v_add_f32_e32 v239, v89, v4
	v_min_f32_e32 v232, 0x40e00000, v232
	v_min_f32_e32 v233, 0x40e00000, v233
	v_min_f32_e32 v234, 0x40e00000, v234
	v_min_f32_e32 v235, 0x40e00000, v235
	v_min_f32_e32 v236, 0x40e00000, v236
	v_min_f32_e32 v237, 0x40e00000, v237
	v_min_f32_e32 v238, 0x40e00000, v238
	v_min_f32_e32 v239, 0x40e00000, v239
	v_mul_f32_e32 v243, 0xc01d265f, v232
	v_mul_f32_e32 v244, 0xc01d265f, v233
	v_mul_f32_e32 v245, 0xc01d265f, v234
	v_mul_f32_e32 v246, 0xc01d265f, v235
	v_mul_f32_e32 v247, 0xc01d265f, v236
	v_mul_f32_e32 v248, 0xc01d265f, v237
	v_mul_f32_e32 v249, 0xc01d265f, v238
	v_mul_f32_e32 v250, 0xc01d265f, v239
	v_exp_f32_e32 v243, v243
	v_exp_f32_e32 v244, v244
	v_exp_f32_e32 v245, v245
	v_exp_f32_e32 v246, v246
	v_exp_f32_e32 v247, v247
	v_exp_f32_e32 v248, v248
	v_exp_f32_e32 v249, v249
	v_exp_f32_e32 v250, v250
	v_add_f32_e32 v202, v58, v15
	v_add_f32_e32 v203, v59, v17
	v_add_f32_e32 v204, v60, v11
	v_add_f32_e32 v205, v61, v13
	v_add_f32_e32 v206, v54, v7
	v_add_f32_e32 v207, v55, v9
	v_add_f32_e32 v208, v56, v3
	v_add_f32_e32 v209, v57, v5
	v_med3_f32 v202, v202, s86, v228
	v_med3_f32 v203, v203, s86, v228
	v_med3_f32 v204, v204, s86, v228
	v_med3_f32 v205, v205, s86, v228
	v_med3_f32 v206, v206, s86, v228
	v_med3_f32 v207, v207, s86, v228
	v_med3_f32 v208, v208, s86, v228
	v_med3_f32 v209, v209, s86, v228
	v_add_f32_e32 v243, 1.0, v243
	v_add_f32_e32 v244, 1.0, v244
	v_add_f32_e32 v245, 1.0, v245
	v_add_f32_e32 v246, 1.0, v246
	v_add_f32_e32 v247, 1.0, v247
	v_add_f32_e32 v248, 1.0, v248
	v_add_f32_e32 v249, 1.0, v249
	v_add_f32_e32 v250, 1.0, v250
	v_rcp_f32_e32 v243, v243
	v_rcp_f32_e32 v244, v244
	v_rcp_f32_e32 v245, v245
	v_rcp_f32_e32 v246, v246
	v_rcp_f32_e32 v247, v247
	v_rcp_f32_e32 v248, v248
	v_rcp_f32_e32 v249, v249
	v_rcp_f32_e32 v250, v250
	v_mul_f32_e32 v232, v232, v243
	v_mul_f32_e32 v233, v233, v244
	v_mul_f32_e32 v234, v234, v245
	v_mul_f32_e32 v235, v235, v246
	v_mul_f32_e32 v236, v236, v247
	v_mul_f32_e32 v237, v237, v248
	v_mul_f32_e32 v238, v238, v249
	v_mul_f32_e32 v239, v239, v250
	v_mul_f32_e32 v232, v202, v232
	v_mul_f32_e32 v233, v203, v233
	v_mul_f32_e32 v234, v204, v234
	v_mul_f32_e32 v235, v205, v235
	v_mul_f32_e32 v236, v206, v236
	v_mul_f32_e32 v237, v207, v237
	v_mul_f32_e32 v238, v208, v238
	v_mul_f32_e32 v239, v209, v239
	v_mov_b32_e32 v212, 0
	v_mov_b32_e32 v213, 0
	v_cvt_pk_fp8_f32 v212, v232, v233
	v_cvt_pk_fp8_f32 v213, v236, v237
	v_cvt_pk_fp8_f32 v212, v234, v235 op_sel:[0,0,1]
	v_cvt_pk_fp8_f32 v213, v238, v239 op_sel:[0,0,1]
	v_add_co_u32_e32 v24, vcc, 0x58000, v18
	s_nop 1
	v_addc_co_u32_e32 v25, vcc, 0, v19, vcc
	global_store_dwordx2 v[24:25], v[212:213], off
	s_andn2_b64 vcc, exec, s[20:21]
	s_cbranch_vccnz .LBB0_1952
;     ...
;         if (!has_next) break;
; #pragma unroll
;         for (int a = 0; a < 2; ++a)
; #pragma unroll
;             for (int b = 0; b < 2; ++b)
; #pragma unroll
;                 for (int m = 0; m < 4; ++m)
; #pragma unroll
;                     for (int n = 0; n < 2; ++n) acc[a][b][m][n] = (f32x4){0.f, 0.f, 0.f, 0.f};
;         cur = nxt; cB = nB; ++ui;
	v_mov_b32_e32 v52, v50
	v_mov_b32_e32 v53, v50
	v_mov_b32_e32 v51, v50
	s_mov_b32 s43, s91
	s_mov_b32 s44, s87
	s_mov_b32 s50, s90
	s_mov_b64 s[6:7], s[26:27]
	s_mov_b32 s88, s89
	s_branch .LBB0_1952

;     ...
;         if (Epi::NST > 0 && ui > 0) { PG_KPAIR(0, 8 + Epi::NST); t0 = 2; }
.LBB0_2899:
	s_cmp_lt_i32 s93, 1
	v_add_u32_e32 v67, 0x10000, v212
	v_add_u32_e32 v68, 0x14000, v212
	v_add_u32_e32 v69, 0x18000, v212
	v_add_u32_e32 v215, 0x1c000, v212
	s_cbranch_scc1 .LBB0_2901
	ds_read_b128 v[2:5], v67
	ds_read_b128 v[6:9], v67 offset:1024
	ds_read_b128 v[10:13], v67 offset:2048
	ds_read_b128 v[14:17], v67 offset:3072
	ds_read_b128 v[18:21], v68
	ds_read_b128 v[22:25], v68 offset:1024
	ds_read_b128 v[26:29], v68 offset:2048
	ds_read_b128 v[30:33], v68 offset:3072
	s_add_u32 s30, s8, 0x100
	s_addc_u32 s31, s9, 0
	ds_read_b128 v[34:37], v213
	ds_read_b128 v[38:41], v213 offset:1024
	ds_read_b128 v[42:45], v213 offset:2048
	ds_read_b128 v[46:49], v213 offset:3072
	ds_read_b128 v[50:53], v213 offset:4096
	ds_read_b128 v[54:57], v213 offset:5120
	ds_read_b128 v[58:61], v213 offset:6144
	ds_read_b128 v[62:65], v213 offset:7168
	s_mov_b32 m0, s64
	s_nop 0
	global_load_lds_dwordx4 v204, s[10:11]
	s_nop 0
	s_mov_b32 m0, s65
	s_nop 0
	global_load_lds_dwordx4 v205, s[10:11]
	s_waitcnt vmcnt(24)
	s_waitcnt lgkmcnt(0)
	s_barrier
	s_setprio 1
	v_mfma_scale_f32_16x16x128_f8f6f4 v[194:197], v[2:9], v[34:41], 0, v211, v211 op_sel_hi:[0,0,0]
	v_mfma_scale_f32_16x16x128_f8f6f4 v[190:193], v[10:17], v[34:41], 0, v211, v211 op_sel_hi:[0,0,0]
	v_mfma_scale_f32_16x16x128_f8f6f4 v[186:189], v[2:9], v[42:49], 0, v211, v211 op_sel_hi:[0,0,0]
	v_mfma_scale_f32_16x16x128_f8f6f4 v[182:185], v[10:17], v[42:49], 0, v211, v211 op_sel_hi:[0,0,0]
	v_mfma_scale_f32_16x16x128_f8f6f4 v[178:181], v[2:9], v[50:57], 0, v211, v211 op_sel_hi:[0,0,0]
	v_mfma_scale_f32_16x16x128_f8f6f4 v[174:177], v[10:17], v[50:57], 0, v211, v211 op_sel_hi:[0,0,0]
	v_mfma_scale_f32_16x16x128_f8f6f4 v[170:173], v[2:9], v[58:65], 0, v211, v211 op_sel_hi:[0,0,0]
	v_mfma_scale_f32_16x16x128_f8f6f4 v[166:169], v[10:17], v[58:65], 0, v211, v211 op_sel_hi:[0,0,0]
	v_mfma_scale_f32_16x16x128_f8f6f4 v[162:165], v[18:25], v[34:41], 0, v211, v211 op_sel_hi:[0,0,0]
	v_mfma_scale_f32_16x16x128_f8f6f4 v[158:161], v[26:33], v[34:41], 0, v211, v211 op_sel_hi:[0,0,0]
	v_mfma_scale_f32_16x16x128_f8f6f4 v[154:157], v[18:25], v[42:49], 0, v211, v211 op_sel_hi:[0,0,0]
	v_mfma_scale_f32_16x16x128_f8f6f4 v[150:153], v[26:33], v[42:49], 0, v211, v211 op_sel_hi:[0,0,0]
	v_mfma_scale_f32_16x16x128_f8f6f4 v[146:149], v[18:25], v[50:57], 0, v211, v211 op_sel_hi:[0,0,0]
	v_mfma_scale_f32_16x16x128_f8f6f4 v[142:145], v[26:33], v[50:57], 0, v211, v211 op_sel_hi:[0,0,0]
	v_mfma_scale_f32_16x16x128_f8f6f4 v[138:141], v[18:25], v[58:65], 0, v211, v211 op_sel_hi:[0,0,0]
	v_mfma_scale_f32_16x16x128_f8f6f4 v[134:137], v[26:33], v[58:65], 0, v211, v211 op_sel_hi:[0,0,0]
	s_setprio 0
	s_barrier
	ds_read_b128 v[34:37], v213 offset:16384
	ds_read_b128 v[38:41], v213 offset:17408
	ds_read_b128 v[42:45], v213 offset:18432
	ds_read_b128 v[46:49], v213 offset:19456
	ds_read_b128 v[50:53], v213 offset:20480
	ds_read_b128 v[54:57], v213 offset:21504
	ds_read_b128 v[58:61], v213 offset:22528
	ds_read_b128 v[62:65], v213 offset:23552
	s_mov_b32 m0, s50
	s_nop 0
	global_load_lds_dwordx4 v198, s[30:31]
	s_nop 0
	s_mov_b32 m0, s51
	s_nop 0
	global_load_lds_dwordx4 v199, s[30:31]
	s_add_u32 s30, s8, 0x40100
	s_addc_u32 s31, s9, 0
	s_mov_b32 m0, s52
	s_nop 0
	global_load_lds_dwordx4 v198, s[30:31]
	s_nop 0
	s_mov_b32 m0, s53
	s_nop 0
	global_load_lds_dwordx4 v199, s[30:31]
	s_nop 0
	s_mov_b32 m0, s49
	s_nop 0
	global_load_lds_dwordx4 v202, s[12:13]
	s_nop 0
	s_mov_b32 m0, s55
	s_nop 0
	global_load_lds_dwordx4 v206, s[12:13]
	s_waitcnt vmcnt(24)
	s_waitcnt lgkmcnt(0)
	s_barrier
	s_setprio 1
	v_mfma_scale_f32_16x16x128_f8f6f4 v[130:133], v[2:9], v[34:41], 0, v211, v211 op_sel_hi:[0,0,0]
	v_mfma_scale_f32_16x16x128_f8f6f4 v[126:129], v[10:17], v[34:41], 0, v211, v211 op_sel_hi:[0,0,0]
	v_mfma_scale_f32_16x16x128_f8f6f4 v[122:125], v[2:9], v[42:49], 0, v211, v211 op_sel_hi:[0,0,0]
	v_mfma_scale_f32_16x16x128_f8f6f4 v[118:121], v[10:17], v[42:49], 0, v211, v211 op_sel_hi:[0,0,0]
	v_mfma_scale_f32_16x16x128_f8f6f4 v[114:117], v[2:9], v[50:57], 0, v211, v211 op_sel_hi:[0,0,0]
	v_mfma_scale_f32_16x16x128_f8f6f4 v[110:113], v[10:17], v[50:57], 0, v211, v211 op_sel_hi:[0,0,0]
	v_mfma_scale_f32_16x16x128_f8f6f4 v[106:109], v[2:9], v[58:65], 0, v211, v211 op_sel_hi:[0,0,0]
	v_mfma_scale_f32_16x16x128_f8f6f4 v[102:105], v[10:17], v[58:65], 0, v211, v211 op_sel_hi:[0,0,0]
	v_mfma_scale_f32_16x16x128_f8f6f4 v[98:101], v[18:25], v[34:41], 0, v211, v211 op_sel_hi:[0,0,0]
	v_mfma_scale_f32_16x16x128_f8f6f4 v[94:97], v[26:33], v[34:41], 0, v211, v211 op_sel_hi:[0,0,0]
	v_mfma_scale_f32_16x16x128_f8f6f4 v[90:93], v[18:25], v[42:49], 0, v211, v211 op_sel_hi:[0,0,0]
	v_mfma_scale_f32_16x16x128_f8f6f4 v[86:89], v[26:33], v[42:49], 0, v211, v211 op_sel_hi:[0,0,0]
	v_mfma_scale_f32_16x16x128_f8f6f4 v[82:85], v[18:25], v[50:57], 0, v211, v211 op_sel_hi:[0,0,0]
	v_mfma_scale_f32_16x16x128_f8f6f4 v[78:81], v[26:33], v[50:57], 0, v211, v211 op_sel_hi:[0,0,0]
	v_mfma_scale_f32_16x16x128_f8f6f4 v[74:77], v[18:25], v[58:65], 0, v211, v211 op_sel_hi:[0,0,0]
	v_mfma_scale_f32_16x16x128_f8f6f4 v[70:73], v[26:33], v[58:65], 0, v211, v211 op_sel_hi:[0,0,0]
	s_setprio 0
	s_barrier
;     ...
;         if (Epi::NST > 0 && ui > 0) { PG_KPAIR(0, 8 + Epi::NST); t0 = 2; }
	ds_read_b128 v[2:5], v69
	ds_read_b128 v[6:9], v69 offset:1024
	ds_read_b128 v[10:13], v69 offset:2048
	ds_read_b128 v[14:17], v69 offset:3072
	ds_read_b128 v[18:21], v215
	ds_read_b128 v[22:25], v215 offset:1024
	ds_read_b128 v[26:29], v215 offset:2048
	ds_read_b128 v[30:33], v215 offset:3072
	ds_read_b128 v[34:37], v213 offset:32768
	ds_read_b128 v[38:41], v213 offset:33792
	ds_read_b128 v[42:45], v213 offset:34816
	ds_read_b128 v[46:49], v213 offset:35840
	ds_read_b128 v[50:53], v213 offset:36864
	ds_read_b128 v[54:57], v213 offset:37888
	ds_read_b128 v[58:61], v213 offset:38912
	ds_read_b128 v[62:65], v213 offset:39936
	s_mov_b32 m0, s56
	s_nop 0
	global_load_lds_dwordx4 v204, s[12:13]
	s_nop 0
	s_mov_b32 m0, s57
	s_nop 0
	global_load_lds_dwordx4 v205, s[12:13]
	s_waitcnt vmcnt(8)
	s_waitcnt lgkmcnt(0)
	s_barrier
	s_setprio 1
	v_mfma_scale_f32_16x16x128_f8f6f4 v[194:197], v[2:9], v[34:41], v[194:197], v211, v211 op_sel_hi:[0,0,0]
	v_mfma_scale_f32_16x16x128_f8f6f4 v[190:193], v[10:17], v[34:41], v[190:193], v211, v211 op_sel_hi:[0,0,0]
	v_mfma_scale_f32_16x16x128_f8f6f4 v[186:189], v[2:9], v[42:49], v[186:189], v211, v211 op_sel_hi:[0,0,0]
	v_mfma_scale_f32_16x16x128_f8f6f4 v[182:185], v[10:17], v[42:49], v[182:185], v211, v211 op_sel_hi:[0,0,0]
	v_mfma_scale_f32_16x16x128_f8f6f4 v[178:181], v[2:9], v[50:57], v[178:181], v211, v211 op_sel_hi:[0,0,0]
	v_mfma_scale_f32_16x16x128_f8f6f4 v[174:177], v[10:17], v[50:57], v[174:177], v211, v211 op_sel_hi:[0,0,0]
	v_mfma_scale_f32_16x16x128_f8f6f4 v[170:173], v[2:9], v[58:65], v[170:173], v211, v211 op_sel_hi:[0,0,0]
	v_mfma_scale_f32_16x16x128_f8f6f4 v[166:169], v[10:17], v[58:65], v[166:169], v211, v211 op_sel_hi:[0,0,0]
	v_mfma_scale_f32_16x16x128_f8f6f4 v[162:165], v[18:25], v[34:41], v[162:165], v211, v211 op_sel_hi:[0,0,0]
	v_mfma_scale_f32_16x16x128_f8f6f4 v[158:161], v[26:33], v[34:41], v[158:161], v211, v211 op_sel_hi:[0,0,0]
	v_mfma_scale_f32_16x16x128_f8f6f4 v[154:157], v[18:25], v[42:49], v[154:157], v211, v211 op_sel_hi:[0,0,0]
	v_mfma_scale_f32_16x16x128_f8f6f4 v[150:153], v[26:33], v[42:49], v[150:153], v211, v211 op_sel_hi:[0,0,0]
	v_mfma_scale_f32_16x16x128_f8f6f4 v[146:149], v[18:25], v[50:57], v[146:149], v211, v211 op_sel_hi:[0,0,0]
	v_mfma_scale_f32_16x16x128_f8f6f4 v[142:145], v[26:33], v[50:57], v[142:145], v211, v211 op_sel_hi:[0,0,0]
	v_mfma_scale_f32_16x16x128_f8f6f4 v[138:141], v[18:25], v[58:65], v[138:141], v211, v211 op_sel_hi:[0,0,0]
	v_mfma_scale_f32_16x16x128_f8f6f4 v[134:137], v[26:33], v[58:65], v[134:137], v211, v211 op_sel_hi:[0,0,0]
	s_setprio 0
	s_barrier
	ds_read_b128 v[34:37], v213 offset:49152
	ds_read_b128 v[38:41], v213 offset:50176
	ds_read_b128 v[42:45], v213 offset:51200
	ds_read_b128 v[46:49], v213 offset:52224
	ds_read_b128 v[50:53], v213 offset:53248
	ds_read_b128 v[54:57], v213 offset:54272
	ds_read_b128 v[58:61], v213 offset:55296
	ds_read_b128 v[62:65], v213 offset:56320
	s_add_u32 s30, s8, 0x180
	s_addc_u32 s31, s9, 0
	s_mov_b32 m0, s58
	s_nop 0
	global_load_lds_dwordx4 v198, s[30:31]
	s_nop 0
	s_mov_b32 m0, s59
	s_nop 0
	global_load_lds_dwordx4 v199, s[30:31]
	s_add_u32 s30, s8, 0x40180
	s_addc_u32 s31, s9, 0
	s_mov_b32 m0, s62
	s_nop 0
	global_load_lds_dwordx4 v198, s[30:31]
	s_nop 0
	s_mov_b32 m0, s63
	s_nop 0
	global_load_lds_dwordx4 v199, s[30:31]
	s_nop 0
	s_mov_b32 m0, s60
	s_nop 0
	global_load_lds_dwordx4 v202, s[14:15]
	s_nop 0
	s_mov_b32 m0, s61
	s_nop 0
	global_load_lds_dwordx4 v206, s[14:15]
	s_waitcnt vmcnt(8)
	s_waitcnt lgkmcnt(0)
	s_barrier
	s_setprio 1
	v_mfma_scale_f32_16x16x128_f8f6f4 v[130:133], v[2:9], v[34:41], v[130:133], v211, v211 op_sel_hi:[0,0,0]
	v_mfma_scale_f32_16x16x128_f8f6f4 v[126:129], v[10:17], v[34:41], v[126:129], v211, v211 op_sel_hi:[0,0,0]
	v_mfma_scale_f32_16x16x128_f8f6f4 v[122:125], v[2:9], v[42:49], v[122:125], v211, v211 op_sel_hi:[0,0,0]
	v_mfma_scale_f32_16x16x128_f8f6f4 v[118:121], v[10:17], v[42:49], v[118:121], v211, v211 op_sel_hi:[0,0,0]
	v_mfma_scale_f32_16x16x128_f8f6f4 v[114:117], v[2:9], v[50:57], v[114:117], v211, v211 op_sel_hi:[0,0,0]
	v_mfma_scale_f32_16x16x128_f8f6f4 v[110:113], v[10:17], v[50:57], v[110:113], v211, v211 op_sel_hi:[0,0,0]
	v_mfma_scale_f32_16x16x128_f8f6f4 v[106:109], v[2:9], v[58:65], v[106:109], v211, v211 op_sel_hi:[0,0,0]
	v_mfma_scale_f32_16x16x128_f8f6f4 v[102:105], v[10:17], v[58:65], v[102:105], v211, v211 op_sel_hi:[0,0,0]
	v_mfma_scale_f32_16x16x128_f8f6f4 v[98:101], v[18:25], v[34:41], v[98:101], v211, v211 op_sel_hi:[0,0,0]
	v_mfma_scale_f32_16x16x128_f8f6f4 v[94:97], v[26:33], v[34:41], v[94:97], v211, v211 op_sel_hi:[0,0,0]
	v_mfma_scale_f32_16x16x128_f8f6f4 v[90:93], v[18:25], v[42:49], v[90:93], v211, v211 op_sel_hi:[0,0,0]
	v_mfma_scale_f32_16x16x128_f8f6f4 v[86:89], v[26:33], v[42:49], v[86:89], v211, v211 op_sel_hi:[0,0,0]
	v_mfma_scale_f32_16x16x128_f8f6f4 v[82:85], v[18:25], v[50:57], v[82:85], v211, v211 op_sel_hi:[0,0,0]
	v_mfma_scale_f32_16x16x128_f8f6f4 v[78:81], v[26:33], v[50:57], v[78:81], v211, v211 op_sel_hi:[0,0,0]
	v_mfma_scale_f32_16x16x128_f8f6f4 v[74:77], v[18:25], v[58:65], v[74:77], v211, v211 op_sel_hi:[0,0,0]
	v_mfma_scale_f32_16x16x128_f8f6f4 v[70:73], v[26:33], v[58:65], v[70:73], v211, v211 op_sel_hi:[0,0,0]
	s_setprio 0
	s_barrier
	s_mov_b32 s34, 2
	s_branch .LBB0_2902

; #define LAS __attribute__((address_space(3)))
; __device__ __forceinline__ unsigned pk4_fp8(float a, float b, float c, float d) { int w = 0; w = __builtin_amdgcn_cvt_pk_fp8_f32(a, b, w, false); w = __builtin_amdgcn_cvt_pk_fp8_f32(c, d, w, true); return (unsigned)w; }
;     __device__ __forceinline__ void operator()(const Acc& acc, const Unit& u, int wr, int wc, int fr, int fq) const {
;         const int row0 = u.pm * 256 + wr * 64 + fr, c0 = u.pn * 256 + wc * 32 + 8 * fq; const LAS float* b2 = bias_lds + (u.ui < 18 ? u.ui : 0) * 256 + wc * 32 + 8 * fq; bf16_t* dst = WSP(bf16_t, WS_Y);
;         f32x4 bv[2][2];
; #pragma unroll
;         for (int bj = 0; bj < 2; ++bj)
; #pragma unroll
;             for (int n = 0; n < 2; ++n) bv[bj][n] = *(const LAS f32x4*)(b2 + bj * 128 + 4 * n) * (Y_FP8 ? Y_SCALE : 1.f);
; #pragma unroll
;         for (int ai = 0; ai < 2; ++ai)
; #pragma unroll
;             for (int m = 0; m < 4; ++m) { const int row = row0 + ai * 128 + m * 16;
; #pragma unroll
;                 for (int bj = 0; bj < 2; ++bj) {
;                     if (Y_FP8) { f32x4 t0 = acc[ai][bj][m][0] * ((MOE_FP8 ? W8_INV : 1.f) * Y_SCALE) + bv[bj][0], t1 = acc[ai][bj][m][1] * ((MOE_FP8 ? W8_INV : 1.f) * Y_SCALE) + bv[bj][1];
; #pragma unroll
;                         for (int j = 0; j < 4; ++j) { t0[j] = __builtin_amdgcn_fmed3f(t0[j], -448.f, 448.f); t1[j] = __builtin_amdgcn_fmed3f(t1[j], -448.f, 448.f); }
;                         u32x2 w; w.x = pk4_fp8(t0[0], t0[1], t0[2], t0[3]); w.y = pk4_fp8(t1[0], t1[1], t1[2], t1[3]);
;                         *(u32x2*)((unsigned char*)dst + (size_t)row * D + c0 + bj * 128) = w; }
.LBB0_2906:
	s_lshl_b32 s2, s54, 8
	s_cmp_lt_i32 s54, 18
	s_cselect_b32 s2, s2, 0
	v_lshl_add_u32 v18, s2, 2, v208
	ds_read_b128 v[2:5], v18
	ds_read_b128 v[14:17], v18 offset:16
	v_lshl_add_u32 v20, s96, 8, v207
	v_ashrrev_i32_e32 v21, 31, v20
	s_mov_b32 s2, 0x40000
	s_waitcnt lgkmcnt(1)
	v_pk_mul_f32 v[12:13], v[2:3], s[20:21] op_sel_hi:[1,0]
	s_waitcnt lgkmcnt(0)
	v_pk_mul_f32 v[6:7], v[16:17], s[20:21] op_sel_hi:[1,0]
	v_pk_mul_f32 v[8:9], v[14:15], s[20:21] op_sel_hi:[1,0]
	ds_read_b128 v[14:17], v18 offset:512
	v_pk_mul_f32 v[10:11], v[4:5], s[20:21] op_sel_hi:[1,0]
	v_pk_fma_f32 v[26:27], v[194:195], s[22:23], v[12:13] op_sel_hi:[1,0,1]
	v_pk_fma_f32 v[24:25], v[196:197], s[22:23], v[10:11] op_sel_hi:[1,0,1]
	v_pk_fma_f32 v[30:31], v[190:191], s[22:23], v[8:9] op_sel_hi:[1,0,1]
	s_waitcnt lgkmcnt(0)
	v_pk_mul_f32 v[2:3], v[16:17], s[20:21] op_sel_hi:[1,0]
	ds_read_b128 v[16:19], v18 offset:528
	v_pk_mul_f32 v[4:5], v[14:15], s[20:21] op_sel_hi:[1,0]
	v_med3_f32 v27, v27, s92, v214
	v_med3_f32 v25, v25, s92, v214
	v_pk_fma_f32 v[28:29], v[192:193], s[22:23], v[6:7] op_sel_hi:[1,0,1]
	s_waitcnt lgkmcnt(0)
	v_pk_mul_f32 v[14:15], v[18:19], s[20:21] op_sel_hi:[1,0]
	v_lshl_or_b32 v18, s46, 8, v210
	v_ashrrev_i32_e32 v19, 31, v18
	v_lshl_add_u64 v[22:23], s[16:17], 0, v[18:19]
	v_lshlrev_b64 v[18:19], 11, v[20:21]
	v_med3_f32 v21, v26, s92, v214
	v_med3_f32 v26, v30, s92, v214
	v_med3_f32 v30, v31, s92, v214
	v_med3_f32 v31, v24, s92, v214
	v_mov_b32_e32 v24, 0
	v_cvt_pk_fp8_f32 v24, v21, v27
	v_med3_f32 v28, v28, s92, v214
	v_med3_f32 v29, v29, s92, v214
	v_pk_mul_f32 v[16:17], v[16:17], s[20:21] op_sel_hi:[1,0]
	v_cvt_pk_fp8_f32 v24, v31, v25 op_sel:[0,0,1]
	v_mov_b32_e32 v25, 0
	v_cvt_pk_fp8_f32 v25, v26, v30
	v_lshl_add_u64 v[18:19], v[22:23], 0, v[18:19]
	v_pk_fma_f32 v[26:27], v[162:163], s[22:23], v[4:5] op_sel_hi:[1,0,1]
	v_pk_fma_f32 v[30:31], v[158:159], s[22:23], v[16:17] op_sel_hi:[1,0,1]
	v_cvt_pk_fp8_f32 v25, v28, v29 op_sel:[0,0,1]
	v_med3_f32 v21, v26, s92, v214
	v_med3_f32 v26, v30, s92, v214
	v_med3_f32 v27, v27, s92, v214
	global_store_dwordx2 v[18:19], v[24:25], off
	v_pk_fma_f32 v[24:25], v[164:165], s[22:23], v[2:3] op_sel_hi:[1,0,1]
	v_med3_f32 v30, v31, s92, v214
	v_med3_f32 v31, v24, s92, v214
	v_mov_b32_e32 v24, 0
	v_cvt_pk_fp8_f32 v24, v21, v27
	v_med3_f32 v25, v25, s92, v214
	v_pk_fma_f32 v[28:29], v[160:161], s[22:23], v[14:15] op_sel_hi:[1,0,1]
	v_pk_fma_f32 v[32:33], v[182:183], s[22:23], v[8:9] op_sel_hi:[1,0,1]
	v_cvt_pk_fp8_f32 v24, v31, v25 op_sel:[0,0,1]
	v_mov_b32_e32 v25, 0
	v_cvt_pk_fp8_f32 v25, v26, v30
	v_med3_f32 v28, v28, s92, v214
	v_med3_f32 v29, v29, s92, v214
	v_pk_fma_f32 v[26:27], v[188:189], s[22:23], v[10:11] op_sel_hi:[1,0,1]
	v_cvt_pk_fp8_f32 v25, v28, v29 op_sel:[0,0,1]
	v_pk_fma_f32 v[28:29], v[186:187], s[22:23], v[12:13] op_sel_hi:[1,0,1]
	v_med3_f32 v27, v27, s92, v214
	v_med3_f32 v21, v28, s92, v214
	v_med3_f32 v28, v32, s92, v214
	v_med3_f32 v29, v29, s92, v214
	v_med3_f32 v32, v33, s92, v214
	v_med3_f32 v33, v26, s92, v214
	v_mov_b32_e32 v26, 0
	v_cvt_pk_fp8_f32 v26, v21, v29
	v_pk_fma_f32 v[30:31], v[184:185], s[22:23], v[6:7] op_sel_hi:[1,0,1]
	global_store_dwordx2 v[18:19], v[24:25], off offset:128
	v_med3_f32 v30, v30, s92, v214
	v_cvt_pk_fp8_f32 v26, v33, v27 op_sel:[0,0,1]
	v_mov_b32_e32 v27, 0
	v_cvt_pk_fp8_f32 v27, v28, v32
	v_med3_f32 v31, v31, s92, v214
	v_or_b32_e32 v24, 16, v20
	v_ashrrev_i32_e32 v25, 31, v24
	v_cvt_pk_fp8_f32 v27, v30, v31 op_sel:[0,0,1]
	v_lshlrev_b64 v[24:25], 11, v[24:25]
	v_lshl_add_u64 v[24:25], v[22:23], 0, v[24:25]
	v_pk_fma_f32 v[28:29], v[154:155], s[22:23], v[4:5] op_sel_hi:[1,0,1]
	global_store_dwordx2 v[24:25], v[26:27], off
	v_pk_fma_f32 v[26:27], v[156:157], s[22:23], v[2:3] op_sel_hi:[1,0,1]
	v_pk_fma_f32 v[32:33], v[150:151], s[22:23], v[16:17] op_sel_hi:[1,0,1]
	v_med3_f32 v21, v28, s92, v214
	v_med3_f32 v28, v32, s92, v214
	v_med3_f32 v29, v29, s92, v214
	v_med3_f32 v32, v33, s92, v214
	v_med3_f32 v33, v26, s92, v214
	v_mov_b32_e32 v26, 0
	v_cvt_pk_fp8_f32 v26, v21, v29
	v_med3_f32 v27, v27, s92, v214
	v_pk_fma_f32 v[30:31], v[152:153], s[22:23], v[14:15] op_sel_hi:[1,0,1]
	s_mov_b64 s[34:35], 0x40000
	v_cvt_pk_fp8_f32 v26, v33, v27 op_sel:[0,0,1]
	v_mov_b32_e32 v27, 0
	v_cvt_pk_fp8_f32 v27, v28, v32
	v_med3_f32 v30, v30, s92, v214
	v_med3_f32 v31, v31, s92, v214
	v_pk_fma_f32 v[28:29], v[178:179], s[22:23], v[12:13] op_sel_hi:[1,0,1]
	v_cvt_pk_fp8_f32 v27, v30, v31 op_sel:[0,0,1]
	v_pk_fma_f32 v[32:33], v[174:175], s[22:23], v[8:9] op_sel_hi:[1,0,1]
	v_med3_f32 v21, v28, s92, v214
	v_med3_f32 v28, v32, s92, v214
	global_store_dwordx2 v[24:25], v[26:27], off offset:128
	v_pk_fma_f32 v[26:27], v[180:181], s[22:23], v[10:11] op_sel_hi:[1,0,1]
	v_med3_f32 v29, v29, s92, v214
	v_med3_f32 v32, v33, s92, v214
	v_med3_f32 v33, v26, s92, v214
	v_mov_b32_e32 v26, 0
	v_cvt_pk_fp8_f32 v26, v21, v29
	v_med3_f32 v27, v27, s92, v214
	v_pk_fma_f32 v[30:31], v[176:177], s[22:23], v[6:7] op_sel_hi:[1,0,1]
	v_or_b32_e32 v24, 32, v20
	v_cvt_pk_fp8_f32 v26, v33, v27 op_sel:[0,0,1]
	v_mov_b32_e32 v27, 0
	v_cvt_pk_fp8_f32 v27, v28, v32
	v_med3_f32 v30, v30, s92, v214
	v_med3_f32 v31, v31, s92, v214
	v_ashrrev_i32_e32 v25, 31, v24
	v_cvt_pk_fp8_f32 v27, v30, v31 op_sel:[0,0,1]
	v_lshlrev_b64 v[24:25], 11, v[24:25]
	v_lshl_add_u64 v[24:25], v[22:23], 0, v[24:25]
	v_pk_fma_f32 v[28:29], v[146:147], s[22:23], v[4:5] op_sel_hi:[1,0,1]
	global_store_dwordx2 v[24:25], v[26:27], off
	v_pk_fma_f32 v[26:27], v[148:149], s[22:23], v[2:3] op_sel_hi:[1,0,1]
	v_pk_fma_f32 v[32:33], v[142:143], s[22:23], v[16:17] op_sel_hi:[1,0,1]
	v_med3_f32 v21, v28, s92, v214
; __device__ __forceinline__ unsigned pk4_fp8(float a, float b, float c, float d) { int w = 0; w = __builtin_amdgcn_cvt_pk_fp8_f32(a, b, w, false); w = __builtin_amdgcn_cvt_pk_fp8_f32(c, d, w, true); return (unsigned)w; }
;     __device__ __forceinline__ void operator()(const Acc& acc, const Unit& u, int wr, int wc, int fr, int fq) const {
;     ...
;             for (int m = 0; m < 4; ++m) { const int row = row0 + ai * 128 + m * 16;
; #pragma unroll
;                 for (int bj = 0; bj < 2; ++bj) {
;                     if (Y_FP8) { f32x4 t0 = acc[ai][bj][m][0] * ((MOE_FP8 ? W8_INV : 1.f) * Y_SCALE) + bv[bj][0], t1 = acc[ai][bj][m][1] * ((MOE_FP8 ? W8_INV : 1.f) * Y_SCALE) + bv[bj][1];
; #pragma unroll
;                         for (int j = 0; j < 4; ++j) { t0[j] = __builtin_amdgcn_fmed3f(t0[j], -448.f, 448.f); t1[j] = __builtin_amdgcn_fmed3f(t1[j], -448.f, 448.f); }
;                         u32x2 w; w.x = pk4_fp8(t0[0], t0[1], t0[2], t0[3]); w.y = pk4_fp8(t1[0], t1[1], t1[2], t1[3]);
;                         *(u32x2*)((unsigned char*)dst + (size_t)row * D + c0 + bj * 128) = w; }
	v_med3_f32 v28, v32, s92, v214
	v_med3_f32 v29, v29, s92, v214
	v_med3_f32 v32, v33, s92, v214
	v_med3_f32 v33, v26, s92, v214
	v_mov_b32_e32 v26, 0
	v_cvt_pk_fp8_f32 v26, v21, v29
	v_med3_f32 v27, v27, s92, v214
	v_pk_fma_f32 v[30:31], v[144:145], s[22:23], v[14:15] op_sel_hi:[1,0,1]
	v_or_b32_e32 v20, 48, v20
	v_cvt_pk_fp8_f32 v26, v33, v27 op_sel:[0,0,1]
	v_mov_b32_e32 v27, 0
	v_cvt_pk_fp8_f32 v27, v28, v32
	v_med3_f32 v30, v30, s92, v214
	v_med3_f32 v31, v31, s92, v214
	v_ashrrev_i32_e32 v21, 31, v20
	v_cvt_pk_fp8_f32 v27, v30, v31 op_sel:[0,0,1]
	v_lshlrev_b64 v[20:21], 11, v[20:21]
	v_lshl_add_u64 v[20:21], v[22:23], 0, v[20:21]
	v_pk_fma_f32 v[22:23], v[172:173], s[22:23], v[10:11] op_sel_hi:[1,0,1]
	global_store_dwordx2 v[24:25], v[26:27], off offset:128
	v_pk_fma_f32 v[24:25], v[170:171], s[22:23], v[12:13] op_sel_hi:[1,0,1]
	v_med3_f32 v30, v22, s92, v214
	v_med3_f32 v24, v24, s92, v214
	v_med3_f32 v25, v25, s92, v214
	v_mov_b32_e32 v22, 0
	v_cvt_pk_fp8_f32 v22, v24, v25
	v_pk_fma_f32 v[28:29], v[166:167], s[22:23], v[8:9] op_sel_hi:[1,0,1]
	v_med3_f32 v23, v23, s92, v214
	v_med3_f32 v28, v28, s92, v214
	v_med3_f32 v29, v29, s92, v214
	v_cvt_pk_fp8_f32 v22, v30, v23 op_sel:[0,0,1]
	v_mov_b32_e32 v23, 0
	v_cvt_pk_fp8_f32 v23, v28, v29
	v_pk_fma_f32 v[26:27], v[168:169], s[22:23], v[6:7] op_sel_hi:[1,0,1]
	v_pk_fma_f32 v[24:25], v[138:139], s[22:23], v[4:5] op_sel_hi:[1,0,1]
	v_med3_f32 v26, v26, s92, v214
	v_med3_f32 v27, v27, s92, v214
	v_cvt_pk_fp8_f32 v23, v26, v27 op_sel:[0,0,1]
	v_med3_f32 v24, v24, s92, v214
	v_med3_f32 v25, v25, s92, v214
	v_pk_fma_f32 v[28:29], v[134:135], s[22:23], v[16:17] op_sel_hi:[1,0,1]
	global_store_dwordx2 v[20:21], v[22:23], off
	v_pk_fma_f32 v[22:23], v[140:141], s[22:23], v[2:3] op_sel_hi:[1,0,1]
	v_med3_f32 v28, v28, s92, v214
	v_med3_f32 v30, v22, s92, v214
	v_mov_b32_e32 v22, 0
	v_cvt_pk_fp8_f32 v22, v24, v25
	v_med3_f32 v23, v23, s92, v214
	v_med3_f32 v29, v29, s92, v214
	v_pk_fma_f32 v[26:27], v[136:137], s[22:23], v[14:15] op_sel_hi:[1,0,1]
	v_cvt_pk_fp8_f32 v22, v30, v23 op_sel:[0,0,1]
	v_mov_b32_e32 v23, 0
	v_cvt_pk_fp8_f32 v23, v28, v29
	v_med3_f32 v26, v26, s92, v214
	v_med3_f32 v27, v27, s92, v214
	v_pk_fma_f32 v[24:25], v[130:131], s[22:23], v[12:13] op_sel_hi:[1,0,1]
	v_cvt_pk_fp8_f32 v23, v26, v27 op_sel:[0,0,1]
	v_med3_f32 v24, v24, s92, v214
	v_med3_f32 v25, v25, s92, v214
	v_pk_fma_f32 v[28:29], v[126:127], s[22:23], v[8:9] op_sel_hi:[1,0,1]
	global_store_dwordx2 v[20:21], v[22:23], off offset:128
	v_pk_fma_f32 v[22:23], v[132:133], s[22:23], v[10:11] op_sel_hi:[1,0,1]
	v_med3_f32 v28, v28, s92, v214
	v_med3_f32 v30, v22, s92, v214
	v_mov_b32_e32 v22, 0
	v_cvt_pk_fp8_f32 v22, v24, v25
	v_med3_f32 v23, v23, s92, v214
	v_med3_f32 v29, v29, s92, v214
	v_pk_fma_f32 v[26:27], v[128:129], s[22:23], v[6:7] op_sel_hi:[1,0,1]
	v_cvt_pk_fp8_f32 v22, v30, v23 op_sel:[0,0,1]
	v_mov_b32_e32 v23, 0
	v_cvt_pk_fp8_f32 v23, v28, v29
	v_med3_f32 v26, v26, s92, v214
	v_med3_f32 v27, v27, s92, v214
	v_add_co_u32_e32 v24, vcc, s2, v18
	v_cvt_pk_fp8_f32 v23, v26, v27 op_sel:[0,0,1]
	s_nop 0
	v_addc_co_u32_e32 v25, vcc, 0, v19, vcc
	v_pk_fma_f32 v[28:29], v[94:95], s[22:23], v[16:17] op_sel_hi:[1,0,1]
	global_store_dwordx2 v[24:25], v[22:23], off
	v_pk_fma_f32 v[22:23], v[100:101], s[22:23], v[2:3] op_sel_hi:[1,0,1]
	v_pk_fma_f32 v[24:25], v[98:99], s[22:23], v[4:5] op_sel_hi:[1,0,1]
	v_med3_f32 v30, v22, s92, v214
	v_med3_f32 v24, v24, s92, v214
	v_med3_f32 v25, v25, s92, v214
	v_mov_b32_e32 v22, 0
	v_cvt_pk_fp8_f32 v22, v24, v25
	v_med3_f32 v23, v23, s92, v214
	v_med3_f32 v28, v28, s92, v214
	v_med3_f32 v29, v29, s92, v214
	v_cvt_pk_fp8_f32 v22, v30, v23 op_sel:[0,0,1]
	v_mov_b32_e32 v23, 0
	v_cvt_pk_fp8_f32 v23, v28, v29
	v_pk_fma_f32 v[26:27], v[96:97], s[22:23], v[14:15] op_sel_hi:[1,0,1]
	v_lshl_add_u64 v[20:21], v[18:19], 0, s[34:35]
	v_med3_f32 v26, v26, s92, v214
	v_med3_f32 v27, v27, s92, v214
	v_cvt_pk_fp8_f32 v23, v26, v27 op_sel:[0,0,1]
	v_pk_fma_f32 v[24:25], v[122:123], s[22:23], v[12:13] op_sel_hi:[1,0,1]
	v_pk_fma_f32 v[28:29], v[118:119], s[22:23], v[8:9] op_sel_hi:[1,0,1]
	v_med3_f32 v24, v24, s92, v214
	global_store_dwordx2 v[20:21], v[22:23], off offset:128
	v_pk_fma_f32 v[22:23], v[124:125], s[22:23], v[10:11] op_sel_hi:[1,0,1]
	v_med3_f32 v25, v25, s92, v214
	v_med3_f32 v30, v22, s92, v214
	v_mov_b32_e32 v22, 0
	v_cvt_pk_fp8_f32 v22, v24, v25
	v_med3_f32 v23, v23, s92, v214
	v_med3_f32 v28, v28, s92, v214
	v_med3_f32 v29, v29, s92, v214
	v_cvt_pk_fp8_f32 v22, v30, v23 op_sel:[0,0,1]
	v_mov_b32_e32 v23, 0
	v_cvt_pk_fp8_f32 v23, v28, v29
	v_pk_fma_f32 v[26:27], v[120:121], s[22:23], v[6:7] op_sel_hi:[1,0,1]
	s_mov_b32 s2, 0x48000
	v_med3_f32 v26, v26, s92, v214
	v_med3_f32 v27, v27, s92, v214
	v_cvt_pk_fp8_f32 v23, v26, v27 op_sel:[0,0,1]
; __device__ __forceinline__ unsigned pk4_fp8(float a, float b, float c, float d) { int w = 0; w = __builtin_amdgcn_cvt_pk_fp8_f32(a, b, w, false); w = __builtin_amdgcn_cvt_pk_fp8_f32(c, d, w, true); return (unsigned)w; }
;     ...
;         if (!has_next) break;
; #pragma unroll
;         for (int a = 0; a < 2; ++a)
; #pragma unroll
;             for (int b = 0; b < 2; ++b)
; #pragma unroll
;                 for (int m = 0; m < 4; ++m)
; #pragma unroll
;                     for (int n = 0; n < 2; ++n) acc[a][b][m][n] = (f32x4){0.f, 0.f, 0.f, 0.f};
;         cur = nxt; cB = nB; ++ui;
;     __device__ __forceinline__ void operator()(const Acc& acc, const Unit& u, int wr, int wc, int fr, int fq) const {
;     ...
;             for (int m = 0; m < 4; ++m) { const int row = row0 + ai * 128 + m * 16;
; #pragma unroll
;                 for (int bj = 0; bj < 2; ++bj) {
;                     if (Y_FP8) { f32x4 t0 = acc[ai][bj][m][0] * ((MOE_FP8 ? W8_INV : 1.f) * Y_SCALE) + bv[bj][0], t1 = acc[ai][bj][m][1] * ((MOE_FP8 ? W8_INV : 1.f) * Y_SCALE) + bv[bj][1];
; #pragma unroll
;                         for (int j = 0; j < 4; ++j) { t0[j] = __builtin_amdgcn_fmed3f(t0[j], -448.f, 448.f); t1[j] = __builtin_amdgcn_fmed3f(t1[j], -448.f, 448.f); }
;                         u32x2 w; w.x = pk4_fp8(t0[0], t0[1], t0[2], t0[3]); w.y = pk4_fp8(t1[0], t1[1], t1[2], t1[3]);
;                         *(u32x2*)((unsigned char*)dst + (size_t)row * D + c0 + bj * 128) = w; }
	v_add_co_u32_e32 v24, vcc, s2, v18
	v_pk_fma_f32 v[28:29], v[86:87], s[22:23], v[16:17] op_sel_hi:[1,0,1]
	s_nop 0
	v_addc_co_u32_e32 v25, vcc, 0, v19, vcc
	global_store_dwordx2 v[24:25], v[22:23], off
	v_pk_fma_f32 v[22:23], v[92:93], s[22:23], v[2:3] op_sel_hi:[1,0,1]
	v_pk_fma_f32 v[24:25], v[90:91], s[22:23], v[4:5] op_sel_hi:[1,0,1]
	v_med3_f32 v30, v22, s92, v214
	v_med3_f32 v24, v24, s92, v214
	v_med3_f32 v25, v25, s92, v214
	v_mov_b32_e32 v22, 0
	v_cvt_pk_fp8_f32 v22, v24, v25
	v_med3_f32 v23, v23, s92, v214
	v_med3_f32 v28, v28, s92, v214
	v_med3_f32 v29, v29, s92, v214
	v_cvt_pk_fp8_f32 v22, v30, v23 op_sel:[0,0,1]
	v_mov_b32_e32 v23, 0
	v_cvt_pk_fp8_f32 v23, v28, v29
	v_pk_fma_f32 v[26:27], v[88:89], s[22:23], v[14:15] op_sel_hi:[1,0,1]
	s_mov_b64 s[34:35], 0x48000
	v_med3_f32 v26, v26, s92, v214
	v_med3_f32 v27, v27, s92, v214
	v_cvt_pk_fp8_f32 v23, v26, v27 op_sel:[0,0,1]
	v_lshl_add_u64 v[20:21], v[18:19], 0, s[34:35]
	v_pk_fma_f32 v[24:25], v[114:115], s[22:23], v[12:13] op_sel_hi:[1,0,1]
	v_pk_fma_f32 v[28:29], v[110:111], s[22:23], v[8:9] op_sel_hi:[1,0,1]
	global_store_dwordx2 v[20:21], v[22:23], off offset:128
	v_pk_fma_f32 v[22:23], v[116:117], s[22:23], v[10:11] op_sel_hi:[1,0,1]
	v_med3_f32 v24, v24, s92, v214
	v_med3_f32 v25, v25, s92, v214
	v_med3_f32 v30, v22, s92, v214
	v_mov_b32_e32 v22, 0
	v_cvt_pk_fp8_f32 v22, v24, v25
	v_med3_f32 v23, v23, s92, v214
	v_med3_f32 v28, v28, s92, v214
	v_med3_f32 v29, v29, s92, v214
	v_cvt_pk_fp8_f32 v22, v30, v23 op_sel:[0,0,1]
	v_mov_b32_e32 v23, 0
	v_cvt_pk_fp8_f32 v23, v28, v29
	v_pk_fma_f32 v[26:27], v[112:113], s[22:23], v[6:7] op_sel_hi:[1,0,1]
	s_mov_b32 s2, 0x50000
	v_med3_f32 v26, v26, s92, v214
	v_med3_f32 v27, v27, s92, v214
	v_cvt_pk_fp8_f32 v23, v26, v27 op_sel:[0,0,1]
	v_add_co_u32_e32 v24, vcc, s2, v18
	v_pk_fma_f32 v[28:29], v[78:79], s[22:23], v[16:17] op_sel_hi:[1,0,1]
	s_nop 0
	v_addc_co_u32_e32 v25, vcc, 0, v19, vcc
	global_store_dwordx2 v[24:25], v[22:23], off
	v_pk_fma_f32 v[22:23], v[84:85], s[22:23], v[2:3] op_sel_hi:[1,0,1]
	v_pk_fma_f32 v[24:25], v[82:83], s[22:23], v[4:5] op_sel_hi:[1,0,1]
	v_med3_f32 v30, v22, s92, v214
	v_med3_f32 v24, v24, s92, v214
	v_med3_f32 v25, v25, s92, v214
	v_mov_b32_e32 v22, 0
	v_cvt_pk_fp8_f32 v22, v24, v25
	v_med3_f32 v23, v23, s92, v214
	v_med3_f32 v28, v28, s92, v214
	v_med3_f32 v29, v29, s92, v214
	v_cvt_pk_fp8_f32 v22, v30, v23 op_sel:[0,0,1]
	v_mov_b32_e32 v23, 0
	v_cvt_pk_fp8_f32 v23, v28, v29
	v_pk_fma_f32 v[26:27], v[80:81], s[22:23], v[14:15] op_sel_hi:[1,0,1]
	s_mov_b64 s[34:35], 0x50000
	v_med3_f32 v26, v26, s92, v214
	v_med3_f32 v27, v27, s92, v214
	v_cvt_pk_fp8_f32 v23, v26, v27 op_sel:[0,0,1]
	v_lshl_add_u64 v[20:21], v[18:19], 0, s[34:35]
	v_pk_fma_f32 v[12:13], v[106:107], s[22:23], v[12:13] op_sel_hi:[1,0,1]
	v_pk_fma_f32 v[6:7], v[104:105], s[22:23], v[6:7] op_sel_hi:[1,0,1]
	v_pk_fma_f32 v[8:9], v[102:103], s[22:23], v[8:9] op_sel_hi:[1,0,1]
	global_store_dwordx2 v[20:21], v[22:23], off offset:128
	v_med3_f32 v12, v12, s92, v214
	v_med3_f32 v8, v8, s92, v214
	v_med3_f32 v13, v13, s92, v214
	v_med3_f32 v9, v9, s92, v214
	v_med3_f32 v22, v6, s92, v214
	v_med3_f32 v23, v7, s92, v214
	v_mov_b32_e32 v6, 0
	v_mov_b32_e32 v7, 0
	v_cvt_pk_fp8_f32 v6, v12, v13
	v_cvt_pk_fp8_f32 v7, v8, v9
	v_pk_fma_f32 v[10:11], v[108:109], s[22:23], v[10:11] op_sel_hi:[1,0,1]
	v_pk_fma_f32 v[2:3], v[76:77], s[22:23], v[2:3] op_sel_hi:[1,0,1]
	v_med3_f32 v10, v10, s92, v214
	v_med3_f32 v11, v11, s92, v214
	v_pk_fma_f32 v[4:5], v[74:75], s[22:23], v[4:5] op_sel_hi:[1,0,1]
	v_cvt_pk_fp8_f32 v6, v10, v11 op_sel:[0,0,1]
	v_cvt_pk_fp8_f32 v7, v22, v23 op_sel:[0,0,1]
	v_med3_f32 v4, v4, s92, v214
	v_med3_f32 v5, v5, s92, v214
	v_med3_f32 v10, v2, s92, v214
	v_mov_b32_e32 v2, 0
	s_mov_b32 s2, 0x58000
	v_cvt_pk_fp8_f32 v2, v4, v5
	v_add_co_u32_e32 v8, vcc, s2, v18
	v_med3_f32 v3, v3, s92, v214
	s_nop 0
	v_addc_co_u32_e32 v9, vcc, 0, v19, vcc
	global_store_dwordx2 v[8:9], v[6:7], off
	v_pk_fma_f32 v[8:9], v[70:71], s[22:23], v[16:17] op_sel_hi:[1,0,1]
	v_cvt_pk_fp8_f32 v2, v10, v3 op_sel:[0,0,1]
	v_med3_f32 v8, v8, s92, v214
	v_med3_f32 v9, v9, s92, v214
	v_mov_b32_e32 v3, 0
	v_cvt_pk_fp8_f32 v3, v8, v9
	v_pk_fma_f32 v[6:7], v[72:73], s[22:23], v[14:15] op_sel_hi:[1,0,1]
	s_mov_b64 s[34:35], 0x58000
	v_med3_f32 v6, v6, s92, v214
	v_med3_f32 v7, v7, s92, v214
	v_cvt_pk_fp8_f32 v3, v6, v7 op_sel:[0,0,1]
	v_lshl_add_u64 v[20:21], v[18:19], 0, s[34:35]
	s_andn2_b64 vcc, exec, s[26:27]
	global_store_dwordx2 v[20:21], v[2:3], off offset:128
	s_cbranch_vccnz .LBB0_2856
	v_mov_b32_e32 v68, v66
	v_mov_b32_e32 v69, v66
	v_mov_b32_e32 v67, v66
	s_mov_b32 s96, s23
	s_mov_b32 s46, s95
	s_mov_b32 s54, s88
	s_mov_b64 s[8:9], s[30:31]
	s_mov_b32 s93, s87
	s_branch .LBB0_2856
